# speedup vs baseline: 1.0275x; 1.0024x over previous
.LBB7_6:
	s_or_b64 exec, exec, s[16:17]
	s_xor_b32 s7, s7, s20
	s_mul_i32 s20, s22, s18
	s_sub_i32 s20, s21, s20
	s_add_i32 s21, s22, 1
	s_sub_i32 s24, s20, s18
	s_cmp_ge_u32 s20, s18
	s_cselect_b32 s21, s21, s22
	s_cselect_b32 s20, s24, s20
	s_add_i32 s22, s21, 1
	s_cmp_ge_u32 s20, s18
	s_cselect_b32 s18, s22, s21
	s_xor_b32 s18, s18, s7
	s_sub_i32 s7, s18, s7
	s_load_dwordx2 s[16:17], s[0:1], 0x10
	s_load_dword s23, s[0:1], 0x28
	s_mul_i32 s3, s7, s3
	s_sub_i32 s3, s19, s3
	v_lshlrev_b32_e32 v2, 3, v0
	s_mul_i32 s18, s7, s5
	s_lshl_b32 s3, s3, 6
	v_lshrrev_b32_e32 v32, 2, v0
	v_and_b32_e32 v10, 24, v2
	s_ashr_i32 s19, s18, 31
	v_or_b32_e32 v6, s3, v32
	s_ashr_i32 s7, s3, 31
	v_lshl_add_u64 v[2:3], s[18:19], 0, v[10:11]
	s_waitcnt lgkmcnt(0)
	s_mul_i32 s7, s16, s7
	v_mad_u64_u32 v[4:5], s[18:19], s16, v6, v[2:3]
	v_mul_lo_u32 v6, s17, v6
	v_add3_u32 v5, v6, v5, s7
	v_add_u32_e32 v6, s2, v32
	s_add_i32 s7, s4, -1
	v_min_i32_e32 v6, s7, v6
	v_mad_i64_i32 v[6:7], s[16:17], v6, s23, v[2:3]
	v_lshlrev_b64 v[6:7], 1, v[6:7]
	v_lshlrev_b64 v[8:9], 1, v[4:5]
	v_lshl_add_u64 v[4:5], s[12:13], 0, v[6:7]
	global_load_dwordx4 v[70:73], v[4:5], off
	v_lshl_add_u64 v[6:7], s[14:15], 0, v[6:7]
	v_lshl_add_u64 v[2:3], s[8:9], 0, v[8:9]
	global_load_dwordx4 v[74:77], v[6:7], off
	global_load_dwordx4 v[78:81], v[2:3], off
	v_lshl_add_u64 v[8:9], s[10:11], 0, v[8:9]
	global_load_dwordx4 v[82:85], v[8:9], off
	s_load_dwordx2 s[8:9], s[0:1], 0x38
	v_and_b32_e32 v11, 32, v32
	v_mul_u32_u24_e32 v32, 40, v32
	v_lshlrev_b32_e32 v10, 1, v10
	v_bfe_u32 v14, v0, 5, 1
	v_lshl_add_u32 v10, v32, 1, v10
	s_ashr_i32 s7, s5, 31
	s_lshr_b32 s7, s7, 27
	s_add_i32 s5, s5, s7
	s_ashr_i32 s5, s5, 5
	s_add_i32 s7, s5, -1
	s_min_i32 s10, s7, 2
	s_lshl_b32 s10, s10, 5
	s_ashr_i32 s11, s10, 31
	s_lshl_b64 s[10:11], s[10:11], 1
	v_lshl_add_u64 v[16:17], v[2:3], 0, s[10:11]
	global_load_dwordx4 v[18:21], v[2:3], off offset:64
	global_load_dwordx4 v[22:25], v[8:9], off offset:64
	global_load_dwordx4 v[26:29], v[4:5], off offset:64
	global_load_dwordx4 v[34:37], v[6:7], off offset:64
	global_load_dwordx4 v[30:33], v[16:17], off
	v_lshl_add_u64 v[16:17], v[8:9], 0, s[10:11]
	global_load_dwordx4 v[38:41], v[16:17], off
	v_lshl_add_u64 v[16:17], v[4:5], 0, s[10:11]
	global_load_dwordx4 v[42:45], v[16:17], off
	v_lshl_add_u64 v[16:17], v[6:7], 0, s[10:11]
	global_load_dwordx4 v[46:49], v[16:17], off
	v_accvgpr_write_b32 a0, 0
	v_accvgpr_write_b32 a1, 0
	v_accvgpr_write_b32 a2, 0
	v_accvgpr_write_b32 a3, 0
	v_accvgpr_write_b32 a4, 0
	v_accvgpr_write_b32 a5, 0
	v_accvgpr_write_b32 a6, 0
	v_accvgpr_write_b32 a7, 0
	v_accvgpr_write_b32 a8, 0
	v_accvgpr_write_b32 a9, 0
	v_accvgpr_write_b32 a10, 0
	v_accvgpr_write_b32 a11, 0
	v_accvgpr_write_b32 a12, 0
	v_accvgpr_write_b32 a13, 0
	v_accvgpr_write_b32 a14, 0
	v_accvgpr_write_b32 a15, 0
	s_waitcnt vmcnt(11)
	ds_write_b128 v10, v[70:73] offset:10240
	s_waitcnt vmcnt(10)
	ds_write_b128 v10, v[74:77] offset:15360
	s_waitcnt vmcnt(9)
	ds_write_b128 v10, v[78:81]
	s_waitcnt vmcnt(8)
	ds_write_b128 v10, v[82:85] offset:5120
	s_waitcnt lgkmcnt(0)
	s_barrier
	v_lshlrev_b32_e32 v17, 4, v14
	s_movk_i32 s10, 0x50
	v_or_b32_e32 v16, v11, v12
	v_mul_u32_u24_e32 v66, 0x50, v15
	v_mad_u32_u24 v15, v15, s10, v17
	v_mul_u32_u24_e32 v67, 0x50, v16
	v_mad_u32_u24 v16, v16, s10, v17
	ds_read_b128 v[58:61], v15 offset:15360
	ds_read_b128 v[50:53], v15 offset:10240
	ds_read_b128 v[54:57], v16
	ds_read_b128 v[62:65], v16 offset:5120
	s_nop 7
	s_mov_b32 s10, 0
	v_add_u32_e32 v15, v17, v67
	v_add_u32_e32 v16, v17, v66
	s_add_i32 s89, s5, -6
	s_cmp_gt_i32 s10, s89
	s_cbranch_scc1 .Ltail_LBB7x8
.LBB7_8:
	s_waitcnt lgkmcnt(0)
	v_mfma_f32_32x32x16_f16 a[0:15], v[62:65], v[50:53], a[0:15]
	ds_read_b128 v[66:69], v16 offset:10272
	ds_read_b128 v[70:73], v15 offset:5152
	ds_read_b128 v[74:77], v15 offset:32
	s_waitcnt vmcnt(7)
	ds_write_b128 v10, v[18:21] offset:20480
	s_waitcnt vmcnt(6)
	ds_write_b128 v10, v[22:25] offset:25600
	s_waitcnt vmcnt(5)
	ds_write_b128 v10, v[26:29] offset:30720
	v_mfma_f32_32x32x16_f16 a[0:15], v[54:57], v[58:61], a[0:15]
	ds_read_b128 v[62:65], v16 offset:15392
	s_waitcnt vmcnt(4)
	ds_write_b128 v10, v[34:37] offset:35840
	v_mfma_f32_32x32x16_f16 a[0:15], v[54:57], v[50:53], a[0:15]
	s_add_i32 s11, s10, 3
	s_min_i32 s11, s11, s7
	s_lshl_b32 s12, s11, 5
	s_ashr_i32 s13, s12, 31
	s_lshl_b64 s[12:13], s[12:13], 1
	v_lshl_add_u64 v[50:51], v[2:3], 0, s[12:13]
	s_waitcnt lgkmcnt(0)
	s_barrier
	v_lshl_add_u64 v[34:35], v[4:5], 0, s[12:13]
	v_lshl_add_u64 v[36:37], v[8:9], 0, s[12:13]
	global_load_dwordx4 v[18:21], v[50:51], off
	global_load_dwordx4 v[22:25], v[36:37], off
	global_load_dwordx4 v[26:29], v[34:35], off
	v_mfma_f32_32x32x16_f16 a[0:15], v[70:73], v[66:69], a[0:15]
	ds_read_b128 v[50:53], v16 offset:30720
	ds_read_b128 v[54:57], v15 offset:25600
	ds_read_b128 v[58:61], v15 offset:20480
	v_lshl_add_u64 v[34:35], v[6:7], 0, s[12:13]
	global_load_dwordx4 v[34:37], v[34:35], off
	v_mfma_f32_32x32x16_f16 a[0:15], v[74:77], v[62:65], a[0:15]
	ds_read_b128 v[70:73], v16 offset:35840
	v_mfma_f32_32x32x16_f16 a[0:15], v[74:77], v[66:69], a[0:15]
	s_waitcnt lgkmcnt(2)
	v_mfma_f32_32x32x16_f16 a[0:15], v[54:57], v[50:53], a[0:15]
	ds_read_b128 v[66:69], v16 offset:30752
	ds_read_b128 v[74:77], v15 offset:25632
	ds_read_b128 v[78:81], v15 offset:20512
	s_waitcnt vmcnt(7)
	ds_write_b128 v10, v[30:33]
	s_waitcnt vmcnt(6)
	ds_write_b128 v10, v[38:41] offset:5120
	s_waitcnt vmcnt(5)
	ds_write_b128 v10, v[42:45] offset:10240
	s_waitcnt lgkmcnt(6)
	v_mfma_f32_32x32x16_f16 a[0:15], v[58:61], v[70:73], a[0:15]
	ds_read_b128 v[82:85], v16 offset:35872
	s_waitcnt vmcnt(4)
	ds_write_b128 v10, v[46:49] offset:15360
	v_mfma_f32_32x32x16_f16 a[0:15], v[58:61], v[50:53], a[0:15]
	s_add_i32 s11, s10, 4
	s_min_i32 s11, s11, s7
	s_lshl_b32 s12, s11, 5
	s_ashr_i32 s13, s12, 31
	s_lshl_b64 s[12:13], s[12:13], 1
	v_lshl_add_u64 v[50:51], v[2:3], 0, s[12:13]
	s_waitcnt lgkmcnt(0)
	s_barrier
	v_lshl_add_u64 v[46:47], v[4:5], 0, s[12:13]
	v_lshl_add_u64 v[48:49], v[8:9], 0, s[12:13]
	global_load_dwordx4 v[30:33], v[50:51], off
	global_load_dwordx4 v[38:41], v[48:49], off
	global_load_dwordx4 v[42:45], v[46:47], off
	v_mfma_f32_32x32x16_f16 a[0:15], v[74:77], v[66:69], a[0:15]
	ds_read_b128 v[50:53], v16 offset:10240
	ds_read_b128 v[62:65], v15 offset:5120
	ds_read_b128 v[54:57], v15
	v_lshl_add_u64 v[46:47], v[6:7], 0, s[12:13]
	global_load_dwordx4 v[46:49], v[46:47], off
	v_mfma_f32_32x32x16_f16 a[0:15], v[78:81], v[82:85], a[0:15]
	ds_read_b128 v[58:61], v16 offset:15360
	v_mfma_f32_32x32x16_f16 a[0:15], v[78:81], v[66:69], a[0:15]
	s_add_i32 s10, s10, 2
	s_add_i32 s89, s5, -6
	s_cmp_le_i32 s10, s89
	s_cbranch_scc1 .LBB7_8
.Ltail_LBB7x8:
	s_waitcnt lgkmcnt(0)
	v_mfma_f32_32x32x16_f16 a[0:15], v[62:65], v[50:53], a[0:15]
	ds_read_b128 v[66:69], v16 offset:10272
	ds_read_b128 v[70:73], v15 offset:5152
	ds_read_b128 v[74:77], v15 offset:32
	s_waitcnt vmcnt(7)
	ds_write_b128 v10, v[18:21] offset:20480
	s_waitcnt vmcnt(6)
	ds_write_b128 v10, v[22:25] offset:25600
	s_waitcnt vmcnt(5)
	ds_write_b128 v10, v[26:29] offset:30720
	v_mfma_f32_32x32x16_f16 a[0:15], v[54:57], v[58:61], a[0:15]
	ds_read_b128 v[62:65], v16 offset:15392
	s_waitcnt vmcnt(4)
	ds_write_b128 v10, v[34:37] offset:35840
	v_mfma_f32_32x32x16_f16 a[0:15], v[54:57], v[50:53], a[0:15]
	s_add_i32 s11, s10, 3
	s_min_i32 s11, s11, s7
	s_lshl_b32 s12, s11, 5
	s_ashr_i32 s13, s12, 31
	s_lshl_b64 s[12:13], s[12:13], 1
	v_lshl_add_u64 v[50:51], v[2:3], 0, s[12:13]
	s_waitcnt lgkmcnt(0)
	s_barrier
	v_lshl_add_u64 v[34:35], v[4:5], 0, s[12:13]
	v_lshl_add_u64 v[36:37], v[8:9], 0, s[12:13]
	global_load_dwordx4 v[18:21], v[50:51], off
	global_load_dwordx4 v[22:25], v[36:37], off
	global_load_dwordx4 v[26:29], v[34:35], off
	v_mfma_f32_32x32x16_f16 a[0:15], v[70:73], v[66:69], a[0:15]
	ds_read_b128 v[50:53], v16 offset:30720
	ds_read_b128 v[54:57], v15 offset:25600
	ds_read_b128 v[58:61], v15 offset:20480
	v_lshl_add_u64 v[34:35], v[6:7], 0, s[12:13]
	global_load_dwordx4 v[34:37], v[34:35], off
	v_mfma_f32_32x32x16_f16 a[0:15], v[74:77], v[62:65], a[0:15]
	ds_read_b128 v[70:73], v16 offset:35840
	v_mfma_f32_32x32x16_f16 a[0:15], v[74:77], v[66:69], a[0:15]
	s_waitcnt lgkmcnt(2)
	v_mfma_f32_32x32x16_f16 a[0:15], v[54:57], v[50:53], a[0:15]
	ds_read_b128 v[66:69], v16 offset:30752
	ds_read_b128 v[74:77], v15 offset:25632
	ds_read_b128 v[78:81], v15 offset:20512
	s_waitcnt vmcnt(7)
	ds_write_b128 v10, v[30:33]
	s_waitcnt vmcnt(6)
	ds_write_b128 v10, v[38:41] offset:5120
	s_waitcnt vmcnt(5)
	ds_write_b128 v10, v[42:45] offset:10240
	s_waitcnt lgkmcnt(6)
	v_mfma_f32_32x32x16_f16 a[0:15], v[58:61], v[70:73], a[0:15]
	ds_read_b128 v[82:85], v16 offset:35872
	s_waitcnt vmcnt(4)
	ds_write_b128 v10, v[46:49] offset:15360
	v_mfma_f32_32x32x16_f16 a[0:15], v[58:61], v[50:53], a[0:15]
	s_add_i32 s11, s10, 4
	s_min_i32 s11, s11, s7
	s_lshl_b32 s12, s11, 5
	s_ashr_i32 s13, s12, 31
	s_lshl_b64 s[12:13], s[12:13], 1
	v_lshl_add_u64 v[50:51], v[2:3], 0, s[12:13]
	s_waitcnt lgkmcnt(0)
	s_barrier
	v_lshl_add_u64 v[46:47], v[4:5], 0, s[12:13]
	v_lshl_add_u64 v[48:49], v[8:9], 0, s[12:13]
	v_mfma_f32_32x32x16_f16 a[0:15], v[74:77], v[66:69], a[0:15]
	ds_read_b128 v[50:53], v16 offset:10240
	ds_read_b128 v[62:65], v15 offset:5120
	ds_read_b128 v[54:57], v15
	v_lshl_add_u64 v[46:47], v[6:7], 0, s[12:13]
	v_mfma_f32_32x32x16_f16 a[0:15], v[78:81], v[82:85], a[0:15]
	ds_read_b128 v[58:61], v16 offset:15360
	v_mfma_f32_32x32x16_f16 a[0:15], v[78:81], v[66:69], a[0:15]
	s_add_i32 s10, s10, 2
	s_waitcnt lgkmcnt(0)
	v_mfma_f32_32x32x16_f16 a[0:15], v[62:65], v[50:53], a[0:15]
	ds_read_b128 v[66:69], v16 offset:10272
	ds_read_b128 v[70:73], v15 offset:5152
	ds_read_b128 v[74:77], v15 offset:32
	s_waitcnt vmcnt(3)
	ds_write_b128 v10, v[18:21] offset:20480
	s_waitcnt vmcnt(2)
	ds_write_b128 v10, v[22:25] offset:25600
	s_waitcnt vmcnt(1)
	ds_write_b128 v10, v[26:29] offset:30720
	v_mfma_f32_32x32x16_f16 a[0:15], v[54:57], v[58:61], a[0:15]
	ds_read_b128 v[62:65], v16 offset:15392
	s_waitcnt vmcnt(0)
	ds_write_b128 v10, v[34:37] offset:35840
	v_mfma_f32_32x32x16_f16 a[0:15], v[54:57], v[50:53], a[0:15]
	s_add_i32 s11, s10, 3
	s_min_i32 s11, s11, s7
	s_lshl_b32 s12, s11, 5
	s_ashr_i32 s13, s12, 31
	s_lshl_b64 s[12:13], s[12:13], 1
	v_lshl_add_u64 v[50:51], v[2:3], 0, s[12:13]
	s_waitcnt lgkmcnt(0)
	s_barrier
	v_lshl_add_u64 v[34:35], v[4:5], 0, s[12:13]
	v_lshl_add_u64 v[36:37], v[8:9], 0, s[12:13]
	v_mfma_f32_32x32x16_f16 a[0:15], v[70:73], v[66:69], a[0:15]
	ds_read_b128 v[50:53], v16 offset:30720
	ds_read_b128 v[54:57], v15 offset:25600
	ds_read_b128 v[58:61], v15 offset:20480
	v_lshl_add_u64 v[34:35], v[6:7], 0, s[12:13]
	v_mfma_f32_32x32x16_f16 a[0:15], v[74:77], v[62:65], a[0:15]
	ds_read_b128 v[70:73], v16 offset:35840
	v_mfma_f32_32x32x16_f16 a[0:15], v[74:77], v[66:69], a[0:15]
	s_waitcnt lgkmcnt(2)
	v_mfma_f32_32x32x16_f16 a[0:15], v[54:57], v[50:53], a[0:15]
	ds_read_b128 v[66:69], v16 offset:30752
	ds_read_b128 v[74:77], v15 offset:25632
	ds_read_b128 v[78:81], v15 offset:20512
	ds_write_b128 v10, v[30:33]
	ds_write_b128 v10, v[38:41] offset:5120
	ds_write_b128 v10, v[42:45] offset:10240
	s_waitcnt lgkmcnt(6)
	v_mfma_f32_32x32x16_f16 a[0:15], v[58:61], v[70:73], a[0:15]
	ds_read_b128 v[82:85], v16 offset:35872
	ds_write_b128 v10, v[46:49] offset:15360
	v_mfma_f32_32x32x16_f16 a[0:15], v[58:61], v[50:53], a[0:15]
	s_add_i32 s11, s10, 4
	s_min_i32 s11, s11, s7
	s_lshl_b32 s12, s11, 5
	s_ashr_i32 s13, s12, 31
	s_lshl_b64 s[12:13], s[12:13], 1
	v_lshl_add_u64 v[50:51], v[2:3], 0, s[12:13]
	s_waitcnt lgkmcnt(0)
	s_barrier
	v_lshl_add_u64 v[46:47], v[4:5], 0, s[12:13]
	v_lshl_add_u64 v[48:49], v[8:9], 0, s[12:13]
	v_mfma_f32_32x32x16_f16 a[0:15], v[74:77], v[66:69], a[0:15]
	ds_read_b128 v[50:53], v16 offset:10240
	ds_read_b128 v[62:65], v15 offset:5120
	ds_read_b128 v[54:57], v15
	v_lshl_add_u64 v[46:47], v[6:7], 0, s[12:13]
	v_mfma_f32_32x32x16_f16 a[0:15], v[78:81], v[82:85], a[0:15]
	ds_read_b128 v[58:61], v16 offset:15360
	v_mfma_f32_32x32x16_f16 a[0:15], v[78:81], v[66:69], a[0:15]
.LBB7_9:
	s_waitcnt vmcnt(0)
	v_lshrrev_b32_e32 v3, 6, v0
	v_mul_u32_u24_e32 v3, 0x1200, v3
	s_waitcnt vmcnt(6)
	s_nop 5
	v_accvgpr_read_b32 v23, a0
	v_accvgpr_read_b32 v22, a1
	v_lshl_or_b32 v12, v12, 2, v3
	s_movk_i32 s5, 0x240
	v_accvgpr_read_b32 v21, a2
	v_accvgpr_read_b32 v20, a3
	v_fma_f32 v23, s6, v23, v13
	v_mad_u32_u24 v12, v14, s5, v12
	v_fma_f32 v14, s6, v22, v13
	v_accvgpr_read_b32 v19, a4
	v_accvgpr_read_b32 v18, a5
	s_waitcnt lgkmcnt(0)
	s_barrier
	ds_write2_b32 v12, v23, v14 offset1:36
	v_fma_f32 v14, s6, v21, v13
	v_fma_f32 v20, s6, v20, v13
	v_and_b32_e32 v2, 63, v0
	v_accvgpr_read_b32 v17, a6
	v_accvgpr_read_b32 v16, a7
	ds_write2_b32 v12, v14, v20 offset0:72 offset1:108
	v_fma_f32 v14, s6, v19, v13
	v_fma_f32 v18, s6, v18, v13
	v_add_u32_e32 v19, 0x400, v12
	v_lshlrev_b32_e32 v0, 2, v0
	v_accvgpr_read_b32 v15, a8
	v_accvgpr_read_b32 v10, a9
	v_accvgpr_read_b32 v9, a10
	v_accvgpr_read_b32 v8, a11
	v_accvgpr_read_b32 v7, a12
	v_accvgpr_read_b32 v6, a13
	v_accvgpr_read_b32 v5, a14
	v_accvgpr_read_b32 v4, a15
	ds_write2_b32 v19, v14, v18 offset0:32 offset1:68
	v_fma_f32 v14, s6, v17, v13
	v_fma_f32 v16, s6, v16, v13
	v_and_b32_e32 v0, 28, v0
	ds_write2_b32 v19, v14, v16 offset0:104 offset1:140
	v_fma_f32 v14, s6, v15, v13
	v_fma_f32 v10, s6, v10, v13
	v_add_u32_e32 v15, 0x800, v12
	v_fma_f32 v9, s6, v9, v13
	v_fma_f32 v8, s6, v8, v13
	v_fma_f32 v7, s6, v7, v13
	v_fma_f32 v6, s6, v6, v13
	v_fma_f32 v5, s6, v5, v13
	v_fmac_f32_e32 v13, s6, v4
	v_or3_b32 v4, s2, v1, v0
	ds_write2_b32 v15, v9, v8 offset0:136 offset1:172
	v_add_u32_e32 v8, 0xc00, v12
	v_cmp_gt_i32_e32 vcc, s4, v4
	ds_write2_b32 v15, v14, v10 offset0:64 offset1:100
	ds_write2_b32 v8, v7, v6 offset0:96 offset1:132
	ds_write2_b32 v8, v5, v13 offset0:168 offset1:204
	s_and_saveexec_b64 s[4:5], vcc
	s_cbranch_execz .LBB7_11
	s_load_dwordx2 s[0:1], s[0:1], 0x40
	v_add_u32_e32 v4, s3, v11
	v_ashrrev_i32_e32 v5, 31, v4
	s_ashr_i32 s3, s2, 31
	v_lshlrev_b32_e32 v0, 2, v0
	s_waitcnt lgkmcnt(0)
	v_mul_lo_u32 v6, s0, v5
	v_mul_lo_u32 v7, s1, v4
	v_mad_u64_u32 v[4:5], s[4:5], s0, v4, 0
	v_add3_u32 v5, v5, v6, v7
	v_lshl_add_u64 v[4:5], v[4:5], 2, s[8:9]
	v_lshl_add_u64 v[4:5], s[2:3], 2, v[4:5]
	v_lshlrev_b32_e32 v6, 2, v1
	v_mov_b32_e32 v7, 0
	v_lshl_add_u64 v[4:5], v[4:5], 0, v[6:7]
	v_mov_b32_e32 v1, v7
	v_lshrrev_b32_e32 v12, 3, v2
	v_lshl_add_u64 v[8:9], v[4:5], 0, v[0:1]
	v_mul_u32_u24_e32 v1, 0x90, v12
	v_add3_u32 v13, v3, v0, v1
	ds_read_b128 v[0:3], v13
	v_mad_u64_u32 v[4:5], s[2:3], s0, v12, 0
	v_mov_b32_e32 v6, v5
	v_mad_u64_u32 v[6:7], s[2:3], s1, v12, v[6:7]
	v_mov_b32_e32 v5, v6
	v_lshl_add_u64 v[10:11], v[4:5], 2, v[8:9]
	ds_read_b128 v[4:7], v13 offset:1152
	s_waitcnt lgkmcnt(1)
	global_store_dwordx4 v[10:11], v[0:3], off sc1
	s_nop 1
	v_or_b32_e32 v3, 8, v12
	v_mad_u64_u32 v[0:1], s[2:3], s0, v3, 0
	v_mov_b32_e32 v2, v1
	v_mad_u64_u32 v[2:3], s[2:3], s1, v3, v[2:3]
	v_mov_b32_e32 v1, v2
	v_lshl_add_u64 v[0:1], v[0:1], 2, v[8:9]
	s_waitcnt lgkmcnt(0)
	global_store_dwordx4 v[0:1], v[4:7], off sc1
	ds_read_b128 v[0:3], v13 offset:2304
	s_nop 0
	v_or_b32_e32 v7, 16, v12
	v_mad_u64_u32 v[4:5], s[2:3], s0, v7, 0
	v_mov_b32_e32 v6, v5
	v_mad_u64_u32 v[6:7], s[2:3], s1, v7, v[6:7]
	v_mov_b32_e32 v5, v6
	v_lshl_add_u64 v[10:11], v[4:5], 2, v[8:9]
	ds_read_b128 v[4:7], v13 offset:3456
	s_waitcnt lgkmcnt(1)
	global_store_dwordx4 v[10:11], v[0:3], off sc1
	s_nop 1
	v_or_b32_e32 v3, 24, v12
	v_mad_u64_u32 v[0:1], s[2:3], s0, v3, 0
	v_mov_b32_e32 v2, v1
	v_mad_u64_u32 v[2:3], s[0:1], s1, v3, v[2:3]
	v_mov_b32_e32 v1, v2
	v_lshl_add_u64 v[0:1], v[0:1], 2, v[8:9]
	s_waitcnt lgkmcnt(0)
	global_store_dwordx4 v[0:1], v[4:7], off sc1

.LBB8_4:
	s_load_dwordx4 s[32:35], s[0:1], 0x18
	s_load_dword s36, s[0:1], 0x28
	s_load_dwordx4 s[4:7], s[0:1], 0x60
	s_load_dwordx2 s[14:15], s[0:1], 0x10
	s_ashr_i32 s2, s2, 3
	s_add_i32 s2, s3, s2
	s_abs_i32 s3, s2
	s_waitcnt lgkmcnt(0)
	s_mov_b32 s92, s6
	s_mov_b32 s93, s7
	v_cvt_f32_u32_e32 v72, s6
	v_cvt_f32_u32_e32 v73, s7
	v_cvt_f32_u32_e32 v74, s2
	v_rcp_iflag_f32_e32 v72, v72
	v_rcp_iflag_f32_e32 v73, v73
	v_add_f32_e32 v74, 0.5, v74
	s_nop 0
	v_mul_f32_e32 v74, v74, v72
	v_cvt_u32_f32_e32 v74, v74
	v_cvt_f32_u32_e32 v72, v74
	v_add_f32_e32 v72, 0.5, v72
	v_readfirstlane_b32 s94, v74
	v_mul_f32_e32 v72, v72, v73
	v_cvt_u32_f32_e32 v72, v72
	s_mul_i32 s90, s94, s92
	s_sub_i32 s90, s2, s90
	v_readfirstlane_b32 s95, v72
	s_nop 0
	s_mul_i32 s91, s95, s93
	s_sub_i32 s91, s94, s91
	s_mov_b32 s3, s94
	s_mov_b32 s18, s90
	s_mov_b32 s2, s95
	s_mov_b32 s3, s91
	v_lshrrev_b32_e32 v1, 6, v0
	v_lshrrev_b32_e32 v3, 2, v0
	v_mov_b32_e32 v17, 0
	v_and_b32_e32 v12, 31, v0
	v_lshlrev_b32_e32 v2, 3, v0
	s_mul_i32 s6, s2, s4
	s_lshl_b32 s16, s3, 6
	v_and_b32_e32 v16, 24, v2
	s_ashr_i32 s7, s6, 31
	v_or_b32_e32 v6, s16, v3
	s_ashr_i32 s17, s16, 31
	v_lshl_add_u64 v[4:5], s[6:7], 0, v[16:17]
	v_lshlrev_b32_e32 v2, 5, v1
	v_lshl_or_b32 v2, s18, 7, v2
	s_mul_i32 s19, s14, s17
	v_mad_u64_u32 v[4:5], s[2:3], s14, v6, v[4:5]
	v_mul_lo_u32 v6, s15, v6
	v_add3_u32 v5, v6, v5, s19
	v_or_b32_e32 v14, v2, v12
	v_lshlrev_b64 v[6:7], 1, v[4:5]
	v_ashrrev_i32_e32 v15, 31, v14
	v_lshl_add_u64 v[4:5], s[10:11], 0, v[6:7]
	v_lshl_add_u64 v[6:7], s[8:9], 0, v[6:7]
	v_lshl_add_u64 v[14:15], v[14:15], 2, s[12:13]
	global_load_dwordx4 v[78:81], v[6:7], off
	global_load_dwordx4 v[82:85], v[4:5], off
	global_load_dword v13, v[14:15], off
	s_load_dwordx2 s[2:3], s[0:1], 0x38
	s_movk_i32 s9, 0x50
	v_lshlrev_b32_e32 v16, 1, v16
	v_and_b32_e32 v14, 63, v0
	s_nop 7
	v_bfe_u32 v15, v0, 5, 1
	v_mad_u32_u24 v17, v3, s9, v16
	s_mov_b32 s10, s36
	s_lshr_b32 s7, s7, 28
	v_lshl_or_b32 v10, s18, 2, v1
	s_add_i32 s6, s6, s7
	s_ashr_i32 s6, s6, 4
	s_waitcnt lgkmcnt(0)
	s_ashr_i32 s18, s10, 31
	s_lshr_b32 s18, s18, 28
	s_ashr_i32 s8, s4, 31
	s_add_i32 s10, s10, s18
	s_ashr_i32 s7, s6, 31
	s_lshr_b32 s8, s8, 27
	s_ashr_i32 s10, s10, 4
	v_mov_b32_e32 v8, s6
	v_mov_b32_e32 v9, s7
	s_add_i32 s4, s4, s8
	v_mad_i64_i32 v[8:9], s[6:7], v10, s10, v[8:9]
	s_ashr_i32 s4, s4, 5
	v_lshlrev_b64 v[10:11], 10, v[8:9]
	s_add_i32 s8, s4, -1
	v_lshl_or_b32 v10, v14, 4, v10
	s_min_i32 s11, s8, 2
	v_lshl_add_u64 v[8:9], s[32:33], 0, v[10:11]
	global_load_dwordx4 v[30:33], v[6:7], off offset:64
	global_load_dwordx4 v[22:25], v[4:5], off offset:64
	v_lshl_add_u64 v[10:11], s[34:35], 0, v[10:11]
	global_load_dwordx4 v[38:41], v[8:9], off
	global_load_dwordx4 v[18:21], v[8:9], off offset:1024
	global_load_dwordx4 v[54:57], v[10:11], off
	global_load_dwordx4 v[26:29], v[10:11], off offset:1024
	global_load_dwordx4 v[42:45], v[8:9], off offset:2048
	global_load_dwordx4 v[50:53], v[10:11], off offset:2048
	s_lshl_b32 s6, s11, 5
	s_ashr_i32 s7, s6, 31
	s_lshl_b64 s[6:7], s[6:7], 1
	v_lshl_add_u64 v[60:61], v[6:7], 0, s[6:7]
	v_lshl_add_u64 v[58:59], v[4:5], 0, s[6:7]
	global_load_dwordx4 v[46:49], v[60:61], off
	global_load_dwordx4 v[34:37], v[58:59], off
	v_accvgpr_write_b32 a0, 0
	v_accvgpr_write_b32 a1, 0
	v_accvgpr_write_b32 a2, 0
	v_accvgpr_write_b32 a3, 0
	v_accvgpr_write_b32 a4, 0
	v_accvgpr_write_b32 a5, 0
	v_accvgpr_write_b32 a6, 0
	v_accvgpr_write_b32 a7, 0
	v_accvgpr_write_b32 a8, 0
	v_accvgpr_write_b32 a9, 0
	v_accvgpr_write_b32 a10, 0
	v_accvgpr_write_b32 a11, 0
	v_accvgpr_write_b32 a12, 0
	v_accvgpr_write_b32 a13, 0
	v_accvgpr_write_b32 a14, 0
	v_accvgpr_write_b32 a15, 0
	v_accvgpr_write_b32 a16, 0
	v_accvgpr_write_b32 a17, 0
	v_accvgpr_write_b32 a18, 0
	v_accvgpr_write_b32 a19, 0
	v_accvgpr_write_b32 a20, 0
	v_accvgpr_write_b32 a21, 0
	v_accvgpr_write_b32 a22, 0
	v_accvgpr_write_b32 a23, 0
	v_accvgpr_write_b32 a24, 0
	v_accvgpr_write_b32 a25, 0
	v_accvgpr_write_b32 a26, 0
	v_accvgpr_write_b32 a27, 0
	v_accvgpr_write_b32 a28, 0
	v_accvgpr_write_b32 a29, 0
	v_accvgpr_write_b32 a30, 0
	v_accvgpr_write_b32 a31, 0
	s_waitcnt vmcnt(12)
	ds_write_b128 v17, v[78:81]
	s_waitcnt vmcnt(11)
	ds_write_b128 v17, v[82:85] offset:5120
	s_waitcnt lgkmcnt(0)
	s_barrier
	v_mul_u32_u24_e32 v17, 0x50, v3
	v_lshlrev_b32_e32 v3, 4, v15
	v_mad_u32_u24 v70, v12, s9, v3
	ds_read_b128 v[58:61], v70 offset:2560
	ds_read_b128 v[66:69], v70
	ds_read_b128 v[62:65], v70 offset:7680
	ds_read_b128 v[70:73], v70 offset:5120
	v_mul_u32_u24_e32 v74, 0x50, v12
	s_mov_b32 s6, 4
	s_nop 7
	v_add_u32_e32 v3, v3, v74
	v_add_u32_e32 v16, v16, v17
	s_add_i32 s89, s4, -2
	s_cmp_gt_i32 s6, s89
	s_cbranch_scc1 .Ltail_LBB8x6
.LBB8_6:
	s_waitcnt vmcnt(7) lgkmcnt(0)
	v_mfma_f32_32x32x16_f16 a[0:15], v[70:73], v[38:41], a[0:15]
	s_add_i32 s7, s6, -3
	s_min_i32 s7, s7, s8
	s_lshl_b32 s7, s7, 1
	ds_read_b128 v[74:77], v3 offset:5152
	s_or_b32 s10, s7, 1
	s_ashr_i32 s11, s10, 31
	s_lshl_b64 s[10:11], s[10:11], 10
	v_lshl_add_u64 v[90:91], v[8:9], 0, s[10:11]
	v_lshl_add_u64 v[92:93], v[10:11], 0, s[10:11]
	s_waitcnt vmcnt(5)
	v_mfma_f32_32x32x16_f16 a[0:15], v[66:69], v[54:57], a[0:15]
	ds_read_b128 v[70:73], v3 offset:32
	v_mfma_f32_32x32x16_f16 a[0:15], v[66:69], v[38:41], a[0:15]
	ds_read_b128 v[78:81], v3 offset:7712
	ds_write_b128 v16, v[30:33] offset:10240
	global_load_dwordx4 v[82:85], v[90:91], off
	global_load_dwordx4 v[86:89], v[92:93], off
	v_mfma_f32_32x32x16_f16 a[16:31], v[62:65], v[38:41], a[16:31]
	ds_read_b128 v[66:69], v3 offset:2592
	ds_write_b128 v16, v[22:25] offset:15360
	v_mfma_f32_32x32x16_f16 a[16:31], v[58:61], v[54:57], a[16:31]
	v_mfma_f32_32x32x16_f16 a[16:31], v[58:61], v[38:41], a[16:31]
	s_add_i32 s7, s6, -1
	s_min_i32 s7, s7, s8
	s_lshl_b32 s10, s7, 5
	s_ashr_i32 s11, s10, 31
	s_lshl_b64 s[10:11], s[10:11], 1
	v_lshl_add_u64 v[22:23], v[6:7], 0, s[10:11]
	s_waitcnt lgkmcnt(0)
	s_barrier
	global_load_dwordx4 v[30:33], v[22:23], off
	v_mfma_f32_32x32x16_f16 a[0:15], v[74:77], v[18:21], a[0:15]
	s_add_i32 s9, s6, -2
	ds_read_b128 v[58:61], v3 offset:15360
	v_lshl_add_u64 v[22:23], v[4:5], 0, s[10:11]
	s_min_i32 s10, s9, s8
	s_lshl_b32 s10, s10, 1
	s_ashr_i32 s11, s10, 31
	s_lshl_b64 s[12:13], s[10:11], 10
	v_lshl_add_u64 v[90:91], v[8:9], 0, s[12:13]
	v_lshl_add_u64 v[92:93], v[10:11], 0, s[12:13]
	global_load_dwordx4 v[22:25], v[22:23], off
	s_waitcnt vmcnt(8)
	v_mfma_f32_32x32x16_f16 a[0:15], v[70:73], v[26:29], a[0:15]
	ds_read_b128 v[62:65], v3 offset:10240
	v_mfma_f32_32x32x16_f16 a[0:15], v[70:73], v[18:21], a[0:15]
	ds_read_b128 v[74:77], v3 offset:17920
	global_load_dwordx4 v[38:41], v[90:91], off
	global_load_dwordx4 v[54:57], v[92:93], off
	v_mfma_f32_32x32x16_f16 a[16:31], v[78:81], v[18:21], a[16:31]
	ds_read_b128 v[70:73], v3 offset:12800
	v_mfma_f32_32x32x16_f16 a[16:31], v[66:69], v[26:29], a[16:31]
	v_mfma_f32_32x32x16_f16 a[16:31], v[66:69], v[18:21], a[16:31]
	s_waitcnt vmcnt(7) lgkmcnt(3)
	v_mfma_f32_32x32x16_f16 a[0:15], v[58:61], v[42:45], a[0:15]
	ds_read_b128 v[66:69], v3 offset:15392
	s_or_b32 s10, s10, 1
	s_ashr_i32 s11, s10, 31
	s_lshl_b64 s[10:11], s[10:11], 10
	v_lshl_add_u64 v[90:91], v[8:9], 0, s[10:11]
	v_lshl_add_u64 v[92:93], v[10:11], 0, s[10:11]
	s_waitcnt vmcnt(6) lgkmcnt(3)
	v_mfma_f32_32x32x16_f16 a[0:15], v[62:65], v[50:53], a[0:15]
	ds_read_b128 v[58:61], v3 offset:10272
	v_mfma_f32_32x32x16_f16 a[0:15], v[62:65], v[42:45], a[0:15]
	ds_read_b128 v[78:81], v3 offset:17952
	s_waitcnt vmcnt(7)
	ds_write_b128 v16, v[46:49]
	global_load_dwordx4 v[18:21], v[90:91], off
	global_load_dwordx4 v[26:29], v[92:93], off
	s_waitcnt lgkmcnt(5)
	v_mfma_f32_32x32x16_f16 a[16:31], v[74:77], v[42:45], a[16:31]
	ds_read_b128 v[90:93], v3 offset:12832
	s_waitcnt vmcnt(8)
	ds_write_b128 v16, v[34:37] offset:5120
	s_waitcnt lgkmcnt(6)
	v_mfma_f32_32x32x16_f16 a[16:31], v[70:73], v[50:53], a[16:31]
	v_mfma_f32_32x32x16_f16 a[16:31], v[70:73], v[42:45], a[16:31]
	s_min_i32 s10, s6, s8
	s_lshl_b32 s10, s10, 5
	s_ashr_i32 s11, s10, 31
	s_lshl_b64 s[10:11], s[10:11], 1
	v_lshl_add_u64 v[34:35], v[6:7], 0, s[10:11]
	s_waitcnt lgkmcnt(0)
	s_barrier
	global_load_dwordx4 v[46:49], v[34:35], off
	s_waitcnt vmcnt(8)
	v_mfma_f32_32x32x16_f16 a[0:15], v[66:69], v[82:85], a[0:15]
	ds_read_b128 v[70:73], v3 offset:5120
	v_lshl_add_u64 v[34:35], v[4:5], 0, s[10:11]
	s_lshl_b32 s10, s7, 1
	s_ashr_i32 s11, s10, 31
	s_lshl_b64 s[10:11], s[10:11], 10
	v_lshl_add_u64 v[74:75], v[8:9], 0, s[10:11]
	v_lshl_add_u64 v[76:77], v[10:11], 0, s[10:11]
	global_load_dwordx4 v[34:37], v[34:35], off
	s_waitcnt vmcnt(8)
	v_mfma_f32_32x32x16_f16 a[0:15], v[58:61], v[86:89], a[0:15]
	ds_read_b128 v[66:69], v3
	v_mfma_f32_32x32x16_f16 a[0:15], v[58:61], v[82:85], a[0:15]
	ds_read_b128 v[62:65], v3 offset:7680
	global_load_dwordx4 v[42:45], v[74:75], off
	global_load_dwordx4 v[50:53], v[76:77], off
	v_mfma_f32_32x32x16_f16 a[16:31], v[78:81], v[82:85], a[16:31]
	ds_read_b128 v[58:61], v3 offset:2560
	v_mfma_f32_32x32x16_f16 a[16:31], v[90:93], v[86:89], a[16:31]
	v_mfma_f32_32x32x16_f16 a[16:31], v[90:93], v[82:85], a[16:31]
	s_add_i32 s6, s6, 2
	s_add_i32 s89, s4, -2
	s_cmp_le_i32 s6, s89
	s_cbranch_scc1 .LBB8_6
.Ltail_LBB8x6:
	s_waitcnt lgkmcnt(0)
	s_waitcnt vmcnt(7)
	v_mfma_f32_32x32x16_f16 a[0:15], v[70:73], v[38:41], a[0:15]
	s_add_i32 s7, s6, -3
	s_min_i32 s7, s7, s8
	s_lshl_b32 s7, s7, 1
	ds_read_b128 v[74:77], v3 offset:5152
	s_or_b32 s10, s7, 1
	s_ashr_i32 s11, s10, 31
	s_lshl_b64 s[10:11], s[10:11], 10
	v_lshl_add_u64 v[90:91], v[8:9], 0, s[10:11]
	v_lshl_add_u64 v[92:93], v[10:11], 0, s[10:11]
	s_waitcnt vmcnt(5)
	v_mfma_f32_32x32x16_f16 a[0:15], v[66:69], v[54:57], a[0:15]
	ds_read_b128 v[70:73], v3 offset:32
	v_mfma_f32_32x32x16_f16 a[0:15], v[66:69], v[38:41], a[0:15]
	ds_read_b128 v[78:81], v3 offset:7712
	ds_write_b128 v16, v[30:33] offset:10240
	global_load_dwordx4 v[82:85], v[90:91], off
	global_load_dwordx4 v[86:89], v[92:93], off
	v_mfma_f32_32x32x16_f16 a[16:31], v[62:65], v[38:41], a[16:31]
	ds_read_b128 v[66:69], v3 offset:2592
	ds_write_b128 v16, v[22:25] offset:15360
	v_mfma_f32_32x32x16_f16 a[16:31], v[58:61], v[54:57], a[16:31]
	v_mfma_f32_32x32x16_f16 a[16:31], v[58:61], v[38:41], a[16:31]
	s_add_i32 s7, s6, -1
	s_min_i32 s7, s7, s8
	s_lshl_b32 s10, s7, 5
	s_ashr_i32 s11, s10, 31
	s_lshl_b64 s[10:11], s[10:11], 1
	v_lshl_add_u64 v[22:23], v[6:7], 0, s[10:11]
	s_waitcnt lgkmcnt(0)
	s_barrier
	global_load_dwordx4 v[30:33], v[22:23], off
	v_mfma_f32_32x32x16_f16 a[0:15], v[74:77], v[18:21], a[0:15]
	s_add_i32 s9, s6, -2
	ds_read_b128 v[58:61], v3 offset:15360
	v_lshl_add_u64 v[22:23], v[4:5], 0, s[10:11]
	s_min_i32 s10, s9, s8
	s_lshl_b32 s10, s10, 1
	s_ashr_i32 s11, s10, 31
	s_lshl_b64 s[12:13], s[10:11], 10
	v_lshl_add_u64 v[90:91], v[8:9], 0, s[12:13]
	v_lshl_add_u64 v[92:93], v[10:11], 0, s[12:13]
	global_load_dwordx4 v[22:25], v[22:23], off
	s_waitcnt vmcnt(8)
	v_mfma_f32_32x32x16_f16 a[0:15], v[70:73], v[26:29], a[0:15]
	ds_read_b128 v[62:65], v3 offset:10240
	v_mfma_f32_32x32x16_f16 a[0:15], v[70:73], v[18:21], a[0:15]
	ds_read_b128 v[74:77], v3 offset:17920
	global_load_dwordx4 v[38:41], v[90:91], off
	global_load_dwordx4 v[54:57], v[92:93], off
	v_mfma_f32_32x32x16_f16 a[16:31], v[78:81], v[18:21], a[16:31]
	ds_read_b128 v[70:73], v3 offset:12800
	v_mfma_f32_32x32x16_f16 a[16:31], v[66:69], v[26:29], a[16:31]
	v_mfma_f32_32x32x16_f16 a[16:31], v[66:69], v[18:21], a[16:31]
	s_waitcnt lgkmcnt(3)
	s_waitcnt vmcnt(7)
	v_mfma_f32_32x32x16_f16 a[0:15], v[58:61], v[42:45], a[0:15]
	ds_read_b128 v[66:69], v3 offset:15392
	s_or_b32 s10, s10, 1
	s_ashr_i32 s11, s10, 31
	s_lshl_b64 s[10:11], s[10:11], 10
	v_lshl_add_u64 v[90:91], v[8:9], 0, s[10:11]
	v_lshl_add_u64 v[92:93], v[10:11], 0, s[10:11]
	s_waitcnt lgkmcnt(3)
	s_waitcnt vmcnt(6)
	v_mfma_f32_32x32x16_f16 a[0:15], v[62:65], v[50:53], a[0:15]
	ds_read_b128 v[58:61], v3 offset:10272
	v_mfma_f32_32x32x16_f16 a[0:15], v[62:65], v[42:45], a[0:15]
	ds_read_b128 v[78:81], v3 offset:17952
	s_waitcnt vmcnt(7)
	ds_write_b128 v16, v[46:49]
	global_load_dwordx4 v[18:21], v[90:91], off
	global_load_dwordx4 v[26:29], v[92:93], off
	s_waitcnt lgkmcnt(5)
	v_mfma_f32_32x32x16_f16 a[16:31], v[74:77], v[42:45], a[16:31]
	ds_read_b128 v[90:93], v3 offset:12832
	s_waitcnt vmcnt(8)
	ds_write_b128 v16, v[34:37] offset:5120
	s_waitcnt lgkmcnt(6)
	v_mfma_f32_32x32x16_f16 a[16:31], v[70:73], v[50:53], a[16:31]
	v_mfma_f32_32x32x16_f16 a[16:31], v[70:73], v[42:45], a[16:31]
	s_min_i32 s10, s6, s8
	s_lshl_b32 s10, s10, 5
	s_ashr_i32 s11, s10, 31
	s_lshl_b64 s[10:11], s[10:11], 1
	v_lshl_add_u64 v[34:35], v[6:7], 0, s[10:11]
	s_waitcnt lgkmcnt(0)
	s_barrier
	s_waitcnt vmcnt(7)
	v_mfma_f32_32x32x16_f16 a[0:15], v[66:69], v[82:85], a[0:15]
	ds_read_b128 v[70:73], v3 offset:5120
	v_lshl_add_u64 v[34:35], v[4:5], 0, s[10:11]
	s_lshl_b32 s10, s7, 1
	s_ashr_i32 s11, s10, 31
	s_lshl_b64 s[10:11], s[10:11], 10
	v_lshl_add_u64 v[74:75], v[8:9], 0, s[10:11]
	v_lshl_add_u64 v[76:77], v[10:11], 0, s[10:11]
	s_waitcnt vmcnt(6)
	v_mfma_f32_32x32x16_f16 a[0:15], v[58:61], v[86:89], a[0:15]
	ds_read_b128 v[66:69], v3
	v_mfma_f32_32x32x16_f16 a[0:15], v[58:61], v[82:85], a[0:15]
	ds_read_b128 v[62:65], v3 offset:7680
	global_load_dwordx4 v[42:45], v[74:75], off
	global_load_dwordx4 v[50:53], v[76:77], off
	v_mfma_f32_32x32x16_f16 a[16:31], v[78:81], v[82:85], a[16:31]
	ds_read_b128 v[58:61], v3 offset:2560
	v_mfma_f32_32x32x16_f16 a[16:31], v[90:93], v[86:89], a[16:31]
	v_mfma_f32_32x32x16_f16 a[16:31], v[90:93], v[82:85], a[16:31]
	s_add_i32 s6, s6, 2
	s_waitcnt lgkmcnt(0)
	s_waitcnt vmcnt(5)
	v_mfma_f32_32x32x16_f16 a[0:15], v[70:73], v[38:41], a[0:15]
	s_add_i32 s7, s6, -3
	s_min_i32 s7, s7, s8
	s_lshl_b32 s7, s7, 1
	ds_read_b128 v[74:77], v3 offset:5152
	s_or_b32 s10, s7, 1
	s_ashr_i32 s11, s10, 31
	s_lshl_b64 s[10:11], s[10:11], 10
	v_lshl_add_u64 v[90:91], v[8:9], 0, s[10:11]
	v_lshl_add_u64 v[92:93], v[10:11], 0, s[10:11]
	s_waitcnt vmcnt(4)
	v_mfma_f32_32x32x16_f16 a[0:15], v[66:69], v[54:57], a[0:15]
	ds_read_b128 v[70:73], v3 offset:32
	v_mfma_f32_32x32x16_f16 a[0:15], v[66:69], v[38:41], a[0:15]
	ds_read_b128 v[78:81], v3 offset:7712
	ds_write_b128 v16, v[30:33] offset:10240
	global_load_dwordx4 v[82:85], v[90:91], off
	global_load_dwordx4 v[86:89], v[92:93], off
	v_mfma_f32_32x32x16_f16 a[16:31], v[62:65], v[38:41], a[16:31]
	ds_read_b128 v[66:69], v3 offset:2592
	ds_write_b128 v16, v[22:25] offset:15360
	v_mfma_f32_32x32x16_f16 a[16:31], v[58:61], v[54:57], a[16:31]
	v_mfma_f32_32x32x16_f16 a[16:31], v[58:61], v[38:41], a[16:31]
	s_add_i32 s7, s6, -1
	s_min_i32 s7, s7, s8
	s_lshl_b32 s10, s7, 5
	s_ashr_i32 s11, s10, 31
	s_lshl_b64 s[10:11], s[10:11], 1
	v_lshl_add_u64 v[22:23], v[6:7], 0, s[10:11]
	s_waitcnt lgkmcnt(0)
	s_barrier
	s_waitcnt vmcnt(5)
	v_mfma_f32_32x32x16_f16 a[0:15], v[74:77], v[18:21], a[0:15]
	s_add_i32 s9, s6, -2
	ds_read_b128 v[58:61], v3 offset:15360
	v_lshl_add_u64 v[22:23], v[4:5], 0, s[10:11]
	s_min_i32 s10, s9, s8
	s_lshl_b32 s10, s10, 1
	s_ashr_i32 s11, s10, 31
	s_lshl_b64 s[12:13], s[10:11], 10
	v_lshl_add_u64 v[90:91], v[8:9], 0, s[12:13]
	v_lshl_add_u64 v[92:93], v[10:11], 0, s[12:13]
	s_waitcnt vmcnt(4)
	v_mfma_f32_32x32x16_f16 a[0:15], v[70:73], v[26:29], a[0:15]
	ds_read_b128 v[62:65], v3 offset:10240
	v_mfma_f32_32x32x16_f16 a[0:15], v[70:73], v[18:21], a[0:15]
	ds_read_b128 v[74:77], v3 offset:17920
	v_mfma_f32_32x32x16_f16 a[16:31], v[78:81], v[18:21], a[16:31]
	ds_read_b128 v[70:73], v3 offset:12800
	v_mfma_f32_32x32x16_f16 a[16:31], v[66:69], v[26:29], a[16:31]
	v_mfma_f32_32x32x16_f16 a[16:31], v[66:69], v[18:21], a[16:31]
	s_waitcnt lgkmcnt(3)
	s_waitcnt vmcnt(3)
	v_mfma_f32_32x32x16_f16 a[0:15], v[58:61], v[42:45], a[0:15]
	ds_read_b128 v[66:69], v3 offset:15392
	s_or_b32 s10, s10, 1
	s_ashr_i32 s11, s10, 31
	s_lshl_b64 s[10:11], s[10:11], 10
	v_lshl_add_u64 v[90:91], v[8:9], 0, s[10:11]
	v_lshl_add_u64 v[92:93], v[10:11], 0, s[10:11]
	s_waitcnt lgkmcnt(3)
	s_waitcnt vmcnt(2)
	v_mfma_f32_32x32x16_f16 a[0:15], v[62:65], v[50:53], a[0:15]
	ds_read_b128 v[58:61], v3 offset:10272
	v_mfma_f32_32x32x16_f16 a[0:15], v[62:65], v[42:45], a[0:15]
	ds_read_b128 v[78:81], v3 offset:17952
	ds_write_b128 v16, v[46:49]
	s_waitcnt lgkmcnt(5)
	v_mfma_f32_32x32x16_f16 a[16:31], v[74:77], v[42:45], a[16:31]
	ds_read_b128 v[90:93], v3 offset:12832
	ds_write_b128 v16, v[34:37] offset:5120
	s_waitcnt lgkmcnt(6)
	v_mfma_f32_32x32x16_f16 a[16:31], v[70:73], v[50:53], a[16:31]
	v_mfma_f32_32x32x16_f16 a[16:31], v[70:73], v[42:45], a[16:31]
	s_min_i32 s10, s6, s8
	s_lshl_b32 s10, s10, 5
	s_ashr_i32 s11, s10, 31
	s_lshl_b64 s[10:11], s[10:11], 1
	v_lshl_add_u64 v[34:35], v[6:7], 0, s[10:11]
	s_waitcnt lgkmcnt(0)
	s_barrier
	s_waitcnt vmcnt(1)
	v_mfma_f32_32x32x16_f16 a[0:15], v[66:69], v[82:85], a[0:15]
	ds_read_b128 v[70:73], v3 offset:5120
	v_lshl_add_u64 v[34:35], v[4:5], 0, s[10:11]
	s_lshl_b32 s10, s7, 1
	s_ashr_i32 s11, s10, 31
	s_lshl_b64 s[10:11], s[10:11], 10
	v_lshl_add_u64 v[74:75], v[8:9], 0, s[10:11]
	v_lshl_add_u64 v[76:77], v[10:11], 0, s[10:11]
	s_waitcnt vmcnt(0)
	v_mfma_f32_32x32x16_f16 a[0:15], v[58:61], v[86:89], a[0:15]
	ds_read_b128 v[66:69], v3
	v_mfma_f32_32x32x16_f16 a[0:15], v[58:61], v[82:85], a[0:15]
	ds_read_b128 v[62:65], v3 offset:7680
	v_mfma_f32_32x32x16_f16 a[16:31], v[78:81], v[82:85], a[16:31]
	ds_read_b128 v[58:61], v3 offset:2560
	v_mfma_f32_32x32x16_f16 a[16:31], v[90:93], v[86:89], a[16:31]
	v_mfma_f32_32x32x16_f16 a[16:31], v[90:93], v[82:85], a[16:31]
.LBB8_7:
	s_waitcnt vmcnt(0)
	s_load_dwordx2 s[0:1], s[0:1], 0x40
	s_waitcnt vmcnt(7)
	v_mul_u32_u24_e32 v40, 0x2400, v1
	v_accvgpr_read_b32 v39, a0
	v_accvgpr_read_b32 v38, a1
	v_lshl_or_b32 v1, v12, 2, v40
	s_waitcnt lgkmcnt(0)
	s_mul_hi_u32 s4, s0, s16
	s_mul_i32 s6, s0, s17
	s_add_i32 s4, s4, s6
	s_mul_i32 s6, s1, s16
	s_add_i32 s7, s4, s6
	s_movk_i32 s4, 0x240
	s_waitcnt vmcnt(2)
	v_accvgpr_read_b32 v37, a2
	v_accvgpr_read_b32 v36, a3
	s_waitcnt vmcnt(0)
	v_fma_f32 v12, s5, v39, v13
	v_mad_u32_u24 v1, v15, s4, v1
	v_fma_f32 v15, s5, v38, v13
	v_accvgpr_read_b32 v35, a4
	v_accvgpr_read_b32 v34, a5
	s_barrier
	ds_write2_b32 v1, v12, v15 offset1:36
	v_fma_f32 v12, s5, v37, v13
	v_fma_f32 v15, s5, v36, v13
	v_accvgpr_read_b32 v33, a6
	v_accvgpr_read_b32 v32, a7
	ds_write2_b32 v1, v12, v15 offset0:72 offset1:108
	v_fma_f32 v12, s5, v35, v13
	v_fma_f32 v15, s5, v34, v13
	v_add_u32_e32 v34, 0x400, v1
	v_accvgpr_read_b32 v31, a8
	v_accvgpr_read_b32 v30, a9
	ds_write2_b32 v34, v12, v15 offset0:32 offset1:68
	v_fma_f32 v12, s5, v33, v13
	v_fma_f32 v15, s5, v32, v13
	v_accvgpr_read_b32 v29, a10
	v_accvgpr_read_b32 v28, a11
	ds_write2_b32 v34, v12, v15 offset0:104 offset1:140
	v_fma_f32 v12, s5, v31, v13
	v_fma_f32 v15, s5, v30, v13
	v_add_u32_e32 v30, 0x800, v1
	v_accvgpr_read_b32 v27, a12
	v_accvgpr_read_b32 v26, a13
	ds_write2_b32 v30, v12, v15 offset0:64 offset1:100
	v_fma_f32 v12, s5, v29, v13
	v_fma_f32 v15, s5, v28, v13
	v_accvgpr_read_b32 v25, a14
	v_accvgpr_read_b32 v24, a15
	ds_write2_b32 v30, v12, v15 offset0:136 offset1:172
	v_fma_f32 v12, s5, v27, v13
	v_fma_f32 v15, s5, v26, v13
	v_add_u32_e32 v26, 0xc00, v1
	v_accvgpr_read_b32 v23, a16
	v_accvgpr_read_b32 v22, a17
	ds_write2_b32 v26, v12, v15 offset0:96 offset1:132
	v_fma_f32 v12, s5, v25, v13
	v_fma_f32 v15, s5, v24, v13
	v_accvgpr_read_b32 v21, a18
	v_accvgpr_read_b32 v20, a19
	ds_write2_b32 v26, v12, v15 offset0:168 offset1:204
	v_fma_f32 v12, s5, v23, v13
	v_fma_f32 v15, s5, v22, v13
	v_add_u32_e32 v22, 0x1000, v1
	v_accvgpr_read_b32 v19, a20
	v_accvgpr_read_b32 v18, a21
	ds_write2_b32 v22, v12, v15 offset0:128 offset1:164
	v_fma_f32 v12, s5, v21, v13
	v_fma_f32 v15, s5, v20, v13
	v_accvgpr_read_b32 v17, a22
	v_accvgpr_read_b32 v16, a23
	ds_write2_b32 v22, v12, v15 offset0:200 offset1:236
	v_fma_f32 v12, s5, v19, v13
	v_fma_f32 v15, s5, v18, v13
	v_add_u32_e32 v18, 0x1400, v1
	v_accvgpr_read_b32 v11, a24
	v_accvgpr_read_b32 v10, a25
	v_accvgpr_read_b32 v9, a26
	v_accvgpr_read_b32 v8, a27
	v_accvgpr_read_b32 v7, a28
	v_accvgpr_read_b32 v6, a29
	v_accvgpr_read_b32 v5, a30
	v_accvgpr_read_b32 v4, a31
	s_mul_i32 s6, s0, s16
	ds_write2_b32 v18, v12, v15 offset0:160 offset1:196
	v_fma_f32 v12, s5, v17, v13
	v_fma_f32 v15, s5, v16, v13
	v_add_u32_e32 v16, 0x1600, v1
	ds_write2_b32 v16, v12, v15 offset0:104 offset1:140
	v_fma_f32 v11, s5, v11, v13
	v_fma_f32 v10, s5, v10, v13
	v_add_u32_e32 v12, 0x1800, v1
	v_fma_f32 v9, s5, v9, v13
	v_fma_f32 v8, s5, v8, v13
	v_fma_f32 v7, s5, v7, v13
	v_fma_f32 v6, s5, v6, v13
	v_fma_f32 v5, s5, v5, v13
	v_fmac_f32_e32 v13, s5, v4
	s_lshl_b64 s[4:5], s[6:7], 2
	ds_write2_b32 v12, v11, v10 offset0:192 offset1:228
	v_add_u32_e32 v10, 0x1c00, v1
	s_add_u32 s2, s2, s4
	v_ashrrev_i32_e32 v3, 31, v2
	ds_write2_b32 v10, v9, v8 offset0:8 offset1:44
	v_add_u32_e32 v8, 0x1e00, v1
	v_add_u32_e32 v1, 0x2000, v1
	s_addc_u32 s3, s3, s5
	v_lshlrev_b32_e32 v0, 4, v0
	ds_write2_b32 v1, v5, v13 offset0:40 offset1:76
	v_lshl_add_u64 v[2:3], v[2:3], 2, s[2:3]
	v_and_b32_e32 v0, 0x70, v0
	v_mov_b32_e32 v1, 0
	ds_write2_b32 v8, v7, v6 offset0:96 offset1:132
	v_lshrrev_b32_e32 v12, 3, v14
	v_lshl_add_u64 v[8:9], v[2:3], 0, v[0:1]
	v_or_b32_e32 v0, v40, v0
	s_movk_i32 s2, 0x90
	v_mad_u32_u24 v13, v12, s2, v0
	ds_read_b128 v[0:3], v13
	v_mad_u64_u32 v[4:5], s[2:3], s0, v12, 0
	v_mov_b32_e32 v6, v5
	v_mad_u64_u32 v[6:7], s[2:3], s1, v12, v[6:7]
	v_mov_b32_e32 v5, v6
	v_lshl_add_u64 v[10:11], v[4:5], 2, v[8:9]
	ds_read_b128 v[4:7], v13 offset:1152
	s_waitcnt lgkmcnt(1)
	global_store_dwordx4 v[10:11], v[0:3], off sc1
	s_nop 1
	v_or_b32_e32 v3, 8, v12
	v_mad_u64_u32 v[0:1], s[2:3], s0, v3, 0
	v_mov_b32_e32 v2, v1
	v_mad_u64_u32 v[2:3], s[2:3], s1, v3, v[2:3]
	v_mov_b32_e32 v1, v2
	v_lshl_add_u64 v[0:1], v[0:1], 2, v[8:9]
	s_waitcnt lgkmcnt(0)
	global_store_dwordx4 v[0:1], v[4:7], off sc1
	ds_read_b128 v[0:3], v13 offset:2304
	s_nop 0
	v_or_b32_e32 v7, 16, v12
	v_mad_u64_u32 v[4:5], s[2:3], s0, v7, 0
	v_mov_b32_e32 v6, v5
	v_mad_u64_u32 v[6:7], s[2:3], s1, v7, v[6:7]
	v_mov_b32_e32 v5, v6
	v_lshl_add_u64 v[10:11], v[4:5], 2, v[8:9]
	ds_read_b128 v[4:7], v13 offset:3456
	s_waitcnt lgkmcnt(1)
	global_store_dwordx4 v[10:11], v[0:3], off sc1
	s_nop 1
	v_or_b32_e32 v3, 24, v12
	v_mad_u64_u32 v[0:1], s[2:3], s0, v3, 0
	v_mov_b32_e32 v2, v1
	v_mad_u64_u32 v[2:3], s[2:3], s1, v3, v[2:3]
	v_mov_b32_e32 v1, v2
	v_lshl_add_u64 v[0:1], v[0:1], 2, v[8:9]
	s_waitcnt lgkmcnt(0)
	global_store_dwordx4 v[0:1], v[4:7], off sc1
	ds_read_b128 v[0:3], v13 offset:4608
	s_nop 0
	v_or_b32_e32 v7, 32, v12
	v_mad_u64_u32 v[4:5], s[2:3], s0, v7, 0
	v_mov_b32_e32 v6, v5
	v_mad_u64_u32 v[6:7], s[2:3], s1, v7, v[6:7]
	v_mov_b32_e32 v5, v6
	v_lshl_add_u64 v[10:11], v[4:5], 2, v[8:9]
	ds_read_b128 v[4:7], v13 offset:5760
	s_waitcnt lgkmcnt(1)
	global_store_dwordx4 v[10:11], v[0:3], off sc1
	s_nop 1
	v_or_b32_e32 v3, 40, v12
	v_mad_u64_u32 v[0:1], s[2:3], s0, v3, 0
	v_mov_b32_e32 v2, v1
	v_mad_u64_u32 v[2:3], s[2:3], s1, v3, v[2:3]
	v_mov_b32_e32 v1, v2
	v_lshl_add_u64 v[0:1], v[0:1], 2, v[8:9]
	s_waitcnt lgkmcnt(0)
	global_store_dwordx4 v[0:1], v[4:7], off sc1
	ds_read_b128 v[0:3], v13 offset:6912
	s_nop 0
	v_or_b32_e32 v7, 48, v12
	v_mad_u64_u32 v[4:5], s[2:3], s0, v7, 0
	v_mov_b32_e32 v6, v5
	v_mad_u64_u32 v[6:7], s[2:3], s1, v7, v[6:7]
	v_mov_b32_e32 v5, v6
	v_lshl_add_u64 v[10:11], v[4:5], 2, v[8:9]
	ds_read_b128 v[4:7], v13 offset:8064
	s_waitcnt lgkmcnt(1)
	global_store_dwordx4 v[10:11], v[0:3], off sc1
	s_nop 1
	v_or_b32_e32 v3, 56, v12
	v_mad_u64_u32 v[0:1], s[2:3], s0, v3, 0
	v_mov_b32_e32 v2, v1
	v_mad_u64_u32 v[2:3], s[0:1], s1, v3, v[2:3]
	v_mov_b32_e32 v1, v2
	v_lshl_add_u64 v[0:1], v[0:1], 2, v[8:9]
	s_waitcnt lgkmcnt(0)
	global_store_dwordx4 v[0:1], v[4:7], off sc1
	s_endpgm
	s_endpgm
	s_endpgm
	s_endpgm
	s_endpgm
	s_endpgm
	s_endpgm
	s_endpgm
	s_endpgm
	s_endpgm
	s_endpgm
	s_endpgm
	s_endpgm
	s_endpgm
	s_endpgm
	s_endpgm
	s_endpgm
	s_endpgm
	s_endpgm
	s_endpgm
	s_endpgm
	s_endpgm
	s_endpgm
	s_endpgm
	s_endpgm
	s_endpgm
	s_endpgm
	s_endpgm
	s_endpgm
	s_endpgm
	s_endpgm
	s_endpgm
	s_endpgm
	s_endpgm
	s_endpgm
	s_endpgm
	s_endpgm
	s_endpgm
	s_endpgm
	s_endpgm

.LBB11_4:
	s_load_dwordx4 s[4:7], s[0:1], 0x60
	s_load_dword s16, s[0:1], 0x70
	s_ashr_i32 s2, s2, 3
	s_add_i32 s18, s3, s2
	s_abs_i32 s2, s18
	s_waitcnt lgkmcnt(0)
	s_load_dwordx2 s[2:3], s[0:1], 0x10
	s_load_dword s21, s[0:1], 0x28
	s_mov_b32 s92, s7
	s_mov_b32 s93, s16
	v_cvt_f32_u32_e32 v80, s7
	v_cvt_f32_u32_e32 v81, s16
	v_cvt_f32_u32_e32 v82, s18
	v_rcp_iflag_f32_e32 v80, v80
	v_rcp_iflag_f32_e32 v81, v81
	v_add_f32_e32 v82, 0.5, v82
	s_nop 0
	v_mul_f32_e32 v82, v82, v80
	v_cvt_u32_f32_e32 v82, v82
	v_cvt_f32_u32_e32 v80, v82
	v_add_f32_e32 v80, 0.5, v80
	v_readfirstlane_b32 s94, v82
	v_mul_f32_e32 v80, v80, v81
	v_cvt_u32_f32_e32 v80, v80
	s_mul_i32 s90, s94, s92
	s_sub_i32 s90, s18, s90
	v_readfirstlane_b32 s95, v80
	s_nop 0
	s_mul_i32 s7, s95, s93
	s_mov_b32 s19, s94
	s_mov_b32 s18, s90
	s_mov_b32 s17, s95
	v_lshrrev_b32_e32 v13, 2, v0
	v_mov_b32_e32 v31, 0
	v_lshrrev_b32_e32 v10, 1, v0
	v_and_b32_e32 v11, 32, v13
	s_lshl_b32 s16, s18, 6
	v_lshlrev_b32_e32 v1, 3, v0
	s_mul_i32 s18, s17, s5
	s_sub_i32 s7, s19, s7
	v_and_b32_e32 v30, 24, v1
	s_ashr_i32 s19, s18, 31
	s_lshl_b32 s7, s7, 6
	v_lshl_add_u64 v[2:3], s[18:19], 0, v[30:31]
	v_or_b32_e32 v4, s16, v13
	s_add_i32 s18, s4, -1
	v_or_b32_e32 v1, s7, v13
	s_ashr_i32 s20, s7, 31
	v_min_i32_e32 v6, s18, v4
	s_waitcnt lgkmcnt(0)
	s_mul_i32 s20, s2, s20
	v_mad_u64_u32 v[4:5], s[18:19], s2, v1, v[2:3]
	v_mul_lo_u32 v1, s3, v1
	v_mad_i64_i32 v[6:7], s[2:3], v6, s21, v[2:3]
	v_add3_u32 v5, v1, v5, s20
	v_lshlrev_b64 v[6:7], 1, v[6:7]
	v_lshlrev_b64 v[8:9], 1, v[4:5]
	v_lshl_add_u64 v[4:5], s[12:13], 0, v[6:7]
	global_load_dwordx4 v[64:67], v[4:5], off
	v_lshl_add_u64 v[6:7], s[14:15], 0, v[6:7]
	v_lshl_add_u64 v[2:3], s[8:9], 0, v[8:9]
	global_load_dwordx4 v[68:71], v[6:7], off
	global_load_dwordx4 v[72:75], v[2:3], off
	v_lshl_add_u64 v[8:9], s[10:11], 0, v[8:9]
	global_load_dwordx4 v[76:79], v[8:9], off
	s_load_dwordx2 s[8:9], s[0:1], 0x38
	v_mul_u32_u24_e32 v13, 40, v13
	v_lshlrev_b32_e32 v30, 1, v30
	s_mov_b32 s2, 0
	v_and_b32_e32 v1, 31, v0
	s_nop 7
	v_bfe_u32 v12, v0, 5, 1
	v_and_b32_e32 v10, 32, v10
	v_lshl_add_u32 v13, v13, 1, v30
	s_ashr_i32 s3, s5, 31
	s_lshr_b32 s3, s3, 27
	s_add_i32 s3, s5, s3
	s_ashr_i32 s3, s3, 5
	s_add_i32 s5, s3, -1
	s_min_i32 s10, s5, 2
	s_lshl_b32 s10, s10, 5
	s_ashr_i32 s11, s10, 31
	s_lshl_b64 s[10:11], s[10:11], 1
	v_lshl_add_u64 v[14:15], v[2:3], 0, s[10:11]
	global_load_dwordx4 v[16:19], v[2:3], off offset:64
	global_load_dwordx4 v[20:23], v[8:9], off offset:64
	global_load_dwordx4 v[24:27], v[4:5], off offset:64
	global_load_dwordx4 v[32:35], v[6:7], off offset:64
	global_load_dwordx4 v[28:31], v[14:15], off
	v_lshl_add_u64 v[14:15], v[8:9], 0, s[10:11]
	global_load_dwordx4 v[36:39], v[14:15], off
	v_lshl_add_u64 v[14:15], v[4:5], 0, s[10:11]
	global_load_dwordx4 v[40:43], v[14:15], off
	v_lshl_add_u64 v[14:15], v[6:7], 0, s[10:11]
	global_load_dwordx4 v[44:47], v[14:15], off
	v_accvgpr_write_b32 a0, 0
	v_accvgpr_write_b32 a1, 0
	v_accvgpr_write_b32 a2, 0
	v_accvgpr_write_b32 a3, 0
	v_accvgpr_write_b32 a4, 0
	v_accvgpr_write_b32 a5, 0
	v_accvgpr_write_b32 a6, 0
	v_accvgpr_write_b32 a7, 0
	v_accvgpr_write_b32 a8, 0
	v_accvgpr_write_b32 a9, 0
	v_accvgpr_write_b32 a10, 0
	v_accvgpr_write_b32 a11, 0
	v_accvgpr_write_b32 a12, 0
	v_accvgpr_write_b32 a13, 0
	v_accvgpr_write_b32 a14, 0
	v_accvgpr_write_b32 a15, 0
	s_waitcnt vmcnt(11)
	ds_write_b128 v13, v[64:67] offset:10240
	s_waitcnt vmcnt(10)
	ds_write_b128 v13, v[68:71] offset:15360
	s_waitcnt vmcnt(9)
	ds_write_b128 v13, v[72:75]
	s_waitcnt vmcnt(8)
	ds_write_b128 v13, v[76:79] offset:5120
	s_waitcnt lgkmcnt(0)
	s_barrier
	v_or_b32_e32 v15, v10, v1
	v_lshlrev_b32_e32 v64, 4, v12
	s_movk_i32 s10, 0x50
	v_or_b32_e32 v14, v11, v1
	v_mul_u32_u24_e32 v65, 0x50, v15
	v_mad_u32_u24 v15, v15, s10, v64
	v_mul_u32_u24_e32 v66, 0x50, v14
	v_mad_u32_u24 v14, v14, s10, v64
	ds_read_b128 v[56:59], v15 offset:15360
	ds_read_b128 v[48:51], v15 offset:10240
	ds_read_b128 v[52:55], v14
	ds_read_b128 v[60:63], v14 offset:5120
	s_nop 7
	v_add_u32_e32 v14, v64, v66
	v_add_u32_e32 v15, v64, v65
	s_add_i32 s89, s3, -6
	s_cmp_gt_i32 s2, s89
	s_cbranch_scc1 .Ltail_LBB11x6
.LBB11_6:
	s_waitcnt lgkmcnt(0)
	v_mfma_f32_32x32x16_f16 a[0:15], v[60:63], v[48:51], a[0:15]
	ds_read_b128 v[64:67], v15 offset:10272
	ds_read_b128 v[68:71], v14 offset:5152
	ds_read_b128 v[72:75], v14 offset:32
	s_waitcnt vmcnt(7)
	ds_write_b128 v13, v[16:19] offset:20480
	s_waitcnt vmcnt(6)
	ds_write_b128 v13, v[20:23] offset:25600
	s_waitcnt vmcnt(5)
	ds_write_b128 v13, v[24:27] offset:30720
	v_mfma_f32_32x32x16_f16 a[0:15], v[52:55], v[56:59], a[0:15]
	ds_read_b128 v[60:63], v15 offset:15392
	s_waitcnt vmcnt(4)
	ds_write_b128 v13, v[32:35] offset:35840
	v_mfma_f32_32x32x16_f16 a[0:15], v[52:55], v[48:51], a[0:15]
	s_add_i32 s10, s2, 3
	s_min_i32 s10, s10, s5
	s_lshl_b32 s10, s10, 5
	s_ashr_i32 s11, s10, 31
	s_lshl_b64 s[10:11], s[10:11], 1
	v_lshl_add_u64 v[48:49], v[2:3], 0, s[10:11]
	s_waitcnt lgkmcnt(0)
	s_barrier
	v_lshl_add_u64 v[32:33], v[4:5], 0, s[10:11]
	v_lshl_add_u64 v[34:35], v[8:9], 0, s[10:11]
	global_load_dwordx4 v[16:19], v[48:49], off
	global_load_dwordx4 v[20:23], v[34:35], off
	global_load_dwordx4 v[24:27], v[32:33], off
	v_mfma_f32_32x32x16_f16 a[0:15], v[68:71], v[64:67], a[0:15]
	ds_read_b128 v[48:51], v15 offset:30720
	ds_read_b128 v[52:55], v14 offset:25600
	ds_read_b128 v[56:59], v14 offset:20480
	v_lshl_add_u64 v[32:33], v[6:7], 0, s[10:11]
	global_load_dwordx4 v[32:35], v[32:33], off
	v_mfma_f32_32x32x16_f16 a[0:15], v[72:75], v[60:63], a[0:15]
	ds_read_b128 v[68:71], v15 offset:35840
	v_mfma_f32_32x32x16_f16 a[0:15], v[72:75], v[64:67], a[0:15]
	s_waitcnt lgkmcnt(2)
	v_mfma_f32_32x32x16_f16 a[0:15], v[52:55], v[48:51], a[0:15]
	ds_read_b128 v[64:67], v15 offset:30752
	ds_read_b128 v[72:75], v14 offset:25632
	ds_read_b128 v[76:79], v14 offset:20512
	s_waitcnt vmcnt(7)
	ds_write_b128 v13, v[28:31]
	s_waitcnt vmcnt(6)
	ds_write_b128 v13, v[36:39] offset:5120
	s_waitcnt vmcnt(5)
	ds_write_b128 v13, v[40:43] offset:10240
	s_waitcnt lgkmcnt(6)
	v_mfma_f32_32x32x16_f16 a[0:15], v[56:59], v[68:71], a[0:15]
	ds_read_b128 v[80:83], v15 offset:35872
	s_waitcnt vmcnt(4)
	ds_write_b128 v13, v[44:47] offset:15360
	v_mfma_f32_32x32x16_f16 a[0:15], v[56:59], v[48:51], a[0:15]
	s_add_i32 s10, s2, 4
	s_min_i32 s10, s10, s5
	s_lshl_b32 s10, s10, 5
	s_ashr_i32 s11, s10, 31
	s_lshl_b64 s[10:11], s[10:11], 1
	v_lshl_add_u64 v[48:49], v[2:3], 0, s[10:11]
	s_waitcnt lgkmcnt(0)
	s_barrier
	v_lshl_add_u64 v[44:45], v[4:5], 0, s[10:11]
	v_lshl_add_u64 v[46:47], v[8:9], 0, s[10:11]
	global_load_dwordx4 v[28:31], v[48:49], off
	global_load_dwordx4 v[36:39], v[46:47], off
	global_load_dwordx4 v[40:43], v[44:45], off
	v_mfma_f32_32x32x16_f16 a[0:15], v[72:75], v[64:67], a[0:15]
	ds_read_b128 v[48:51], v15 offset:10240
	ds_read_b128 v[60:63], v14 offset:5120
	ds_read_b128 v[52:55], v14
	v_lshl_add_u64 v[44:45], v[6:7], 0, s[10:11]
	global_load_dwordx4 v[44:47], v[44:45], off
	v_mfma_f32_32x32x16_f16 a[0:15], v[76:79], v[80:83], a[0:15]
	ds_read_b128 v[56:59], v15 offset:15360
	v_mfma_f32_32x32x16_f16 a[0:15], v[76:79], v[64:67], a[0:15]
	s_add_i32 s2, s2, 2
	s_add_i32 s89, s3, -6
	s_cmp_le_i32 s2, s89
	s_cbranch_scc1 .LBB11_6
.Ltail_LBB11x6:
	s_waitcnt lgkmcnt(0)
	v_mfma_f32_32x32x16_f16 a[0:15], v[60:63], v[48:51], a[0:15]
	ds_read_b128 v[64:67], v15 offset:10272
	ds_read_b128 v[68:71], v14 offset:5152
	ds_read_b128 v[72:75], v14 offset:32
	s_waitcnt vmcnt(7)
	ds_write_b128 v13, v[16:19] offset:20480
	s_waitcnt vmcnt(6)
	ds_write_b128 v13, v[20:23] offset:25600
	s_waitcnt vmcnt(5)
	ds_write_b128 v13, v[24:27] offset:30720
	v_mfma_f32_32x32x16_f16 a[0:15], v[52:55], v[56:59], a[0:15]
	ds_read_b128 v[60:63], v15 offset:15392
	s_waitcnt vmcnt(4)
	ds_write_b128 v13, v[32:35] offset:35840
	v_mfma_f32_32x32x16_f16 a[0:15], v[52:55], v[48:51], a[0:15]
	s_add_i32 s10, s2, 3
	s_min_i32 s10, s10, s5
	s_lshl_b32 s10, s10, 5
	s_ashr_i32 s11, s10, 31
	s_lshl_b64 s[10:11], s[10:11], 1
	v_lshl_add_u64 v[48:49], v[2:3], 0, s[10:11]
	s_waitcnt lgkmcnt(0)
	s_barrier
	v_lshl_add_u64 v[32:33], v[4:5], 0, s[10:11]
	v_lshl_add_u64 v[34:35], v[8:9], 0, s[10:11]
	global_load_dwordx4 v[16:19], v[48:49], off
	global_load_dwordx4 v[20:23], v[34:35], off
	global_load_dwordx4 v[24:27], v[32:33], off
	v_mfma_f32_32x32x16_f16 a[0:15], v[68:71], v[64:67], a[0:15]
	ds_read_b128 v[48:51], v15 offset:30720
	ds_read_b128 v[52:55], v14 offset:25600
	ds_read_b128 v[56:59], v14 offset:20480
	v_lshl_add_u64 v[32:33], v[6:7], 0, s[10:11]
	global_load_dwordx4 v[32:35], v[32:33], off
	v_mfma_f32_32x32x16_f16 a[0:15], v[72:75], v[60:63], a[0:15]
	ds_read_b128 v[68:71], v15 offset:35840
	v_mfma_f32_32x32x16_f16 a[0:15], v[72:75], v[64:67], a[0:15]
	s_waitcnt lgkmcnt(2)
	v_mfma_f32_32x32x16_f16 a[0:15], v[52:55], v[48:51], a[0:15]
	ds_read_b128 v[64:67], v15 offset:30752
	ds_read_b128 v[72:75], v14 offset:25632
	ds_read_b128 v[76:79], v14 offset:20512
	s_waitcnt vmcnt(7)
	ds_write_b128 v13, v[28:31]
	s_waitcnt vmcnt(6)
	ds_write_b128 v13, v[36:39] offset:5120
	s_waitcnt vmcnt(5)
	ds_write_b128 v13, v[40:43] offset:10240
	s_waitcnt lgkmcnt(6)
	v_mfma_f32_32x32x16_f16 a[0:15], v[56:59], v[68:71], a[0:15]
	ds_read_b128 v[80:83], v15 offset:35872
	s_waitcnt vmcnt(4)
	ds_write_b128 v13, v[44:47] offset:15360
	v_mfma_f32_32x32x16_f16 a[0:15], v[56:59], v[48:51], a[0:15]
	s_add_i32 s10, s2, 4
	s_min_i32 s10, s10, s5
	s_lshl_b32 s10, s10, 5
	s_ashr_i32 s11, s10, 31
	s_lshl_b64 s[10:11], s[10:11], 1
	v_lshl_add_u64 v[48:49], v[2:3], 0, s[10:11]
	s_waitcnt lgkmcnt(0)
	s_barrier
	v_lshl_add_u64 v[44:45], v[4:5], 0, s[10:11]
	v_lshl_add_u64 v[46:47], v[8:9], 0, s[10:11]
	v_mfma_f32_32x32x16_f16 a[0:15], v[72:75], v[64:67], a[0:15]
	ds_read_b128 v[48:51], v15 offset:10240
	ds_read_b128 v[60:63], v14 offset:5120
	ds_read_b128 v[52:55], v14
	v_lshl_add_u64 v[44:45], v[6:7], 0, s[10:11]
	v_mfma_f32_32x32x16_f16 a[0:15], v[76:79], v[80:83], a[0:15]
	ds_read_b128 v[56:59], v15 offset:15360
	v_mfma_f32_32x32x16_f16 a[0:15], v[76:79], v[64:67], a[0:15]
	s_add_i32 s2, s2, 2
	s_waitcnt lgkmcnt(0)
	v_mfma_f32_32x32x16_f16 a[0:15], v[60:63], v[48:51], a[0:15]
	ds_read_b128 v[64:67], v15 offset:10272
	ds_read_b128 v[68:71], v14 offset:5152
	ds_read_b128 v[72:75], v14 offset:32
	s_waitcnt vmcnt(3)
	ds_write_b128 v13, v[16:19] offset:20480
	s_waitcnt vmcnt(2)
	ds_write_b128 v13, v[20:23] offset:25600
	s_waitcnt vmcnt(1)
	ds_write_b128 v13, v[24:27] offset:30720
	v_mfma_f32_32x32x16_f16 a[0:15], v[52:55], v[56:59], a[0:15]
	ds_read_b128 v[60:63], v15 offset:15392
	s_waitcnt vmcnt(0)
	ds_write_b128 v13, v[32:35] offset:35840
	v_mfma_f32_32x32x16_f16 a[0:15], v[52:55], v[48:51], a[0:15]
	s_add_i32 s10, s2, 3
	s_min_i32 s10, s10, s5
	s_lshl_b32 s10, s10, 5
	s_ashr_i32 s11, s10, 31
	s_lshl_b64 s[10:11], s[10:11], 1
	v_lshl_add_u64 v[48:49], v[2:3], 0, s[10:11]
	s_waitcnt lgkmcnt(0)
	s_barrier
	v_lshl_add_u64 v[32:33], v[4:5], 0, s[10:11]
	v_lshl_add_u64 v[34:35], v[8:9], 0, s[10:11]
	v_mfma_f32_32x32x16_f16 a[0:15], v[68:71], v[64:67], a[0:15]
	ds_read_b128 v[48:51], v15 offset:30720
	ds_read_b128 v[52:55], v14 offset:25600
	ds_read_b128 v[56:59], v14 offset:20480
	v_lshl_add_u64 v[32:33], v[6:7], 0, s[10:11]
	v_mfma_f32_32x32x16_f16 a[0:15], v[72:75], v[60:63], a[0:15]
	ds_read_b128 v[68:71], v15 offset:35840
	v_mfma_f32_32x32x16_f16 a[0:15], v[72:75], v[64:67], a[0:15]
	s_waitcnt lgkmcnt(2)
	v_mfma_f32_32x32x16_f16 a[0:15], v[52:55], v[48:51], a[0:15]
	ds_read_b128 v[64:67], v15 offset:30752
	ds_read_b128 v[72:75], v14 offset:25632
	ds_read_b128 v[76:79], v14 offset:20512
	ds_write_b128 v13, v[28:31]
	ds_write_b128 v13, v[36:39] offset:5120
	ds_write_b128 v13, v[40:43] offset:10240
	s_waitcnt lgkmcnt(6)
	v_mfma_f32_32x32x16_f16 a[0:15], v[56:59], v[68:71], a[0:15]
	ds_read_b128 v[80:83], v15 offset:35872
	ds_write_b128 v13, v[44:47] offset:15360
	v_mfma_f32_32x32x16_f16 a[0:15], v[56:59], v[48:51], a[0:15]
	s_add_i32 s10, s2, 4
	s_min_i32 s10, s10, s5
	s_lshl_b32 s10, s10, 5
	s_ashr_i32 s11, s10, 31
	s_lshl_b64 s[10:11], s[10:11], 1
	v_lshl_add_u64 v[48:49], v[2:3], 0, s[10:11]
	s_waitcnt lgkmcnt(0)
	s_barrier
	v_lshl_add_u64 v[44:45], v[4:5], 0, s[10:11]
	v_lshl_add_u64 v[46:47], v[8:9], 0, s[10:11]
	v_mfma_f32_32x32x16_f16 a[0:15], v[72:75], v[64:67], a[0:15]
	ds_read_b128 v[48:51], v15 offset:10240
	ds_read_b128 v[60:63], v14 offset:5120
	ds_read_b128 v[52:55], v14
	v_lshl_add_u64 v[44:45], v[6:7], 0, s[10:11]
	v_mfma_f32_32x32x16_f16 a[0:15], v[76:79], v[80:83], a[0:15]
	ds_read_b128 v[56:59], v15 offset:15360
	v_mfma_f32_32x32x16_f16 a[0:15], v[76:79], v[64:67], a[0:15]
.LBB11_7:
	s_waitcnt vmcnt(0)
	v_lshrrev_b32_e32 v3, 6, v0
	v_mul_u32_u24_e32 v3, 0x1200, v3
	s_waitcnt vmcnt(6)
	s_nop 5
	v_accvgpr_read_b32 v20, a2
	v_accvgpr_read_b32 v19, a3
	v_lshl_or_b32 v23, v1, 2, v3
	s_movk_i32 s2, 0x240
	v_accvgpr_read_b32 v16, a6
	v_accvgpr_read_b32 v15, a7
	v_mad_u32_u24 v12, v12, s2, v23
	v_fma_f32 v20, s6, v20, 0
	v_fma_f32 v19, s6, v19, 0
	v_accvgpr_read_b32 v9, a10
	v_accvgpr_read_b32 v8, a11
	s_waitcnt lgkmcnt(0)
	s_barrier
	ds_write2_b32 v12, v20, v19 offset0:72 offset1:108
	v_add_u32_e32 v19, 0x400, v12
	v_fma_f32 v16, s6, v16, 0
	v_fma_f32 v15, s6, v15, 0
	v_and_b32_e32 v2, 63, v0
	v_accvgpr_read_b32 v5, a14
	v_accvgpr_read_b32 v4, a15
	ds_write2_b32 v19, v16, v15 offset0:104 offset1:140
	v_add_u32_e32 v15, 0x800, v12
	v_fma_f32 v9, s6, v9, 0
	v_fma_f32 v8, s6, v8, 0
	v_lshlrev_b32_e32 v0, 2, v0
	ds_write2_b32 v15, v9, v8 offset0:136 offset1:172
	v_add_u32_e32 v8, 0xc00, v12
	v_fma_f32 v5, s6, v5, 0
	v_fma_f32 v4, s6, v4, 0
	v_and_b32_e32 v0, 28, v0
	v_accvgpr_read_b32 v22, a0
	v_accvgpr_read_b32 v21, a1
	v_accvgpr_read_b32 v18, a4
	v_accvgpr_read_b32 v17, a5
	v_accvgpr_read_b32 v14, a8
	v_accvgpr_read_b32 v13, a9
	v_accvgpr_read_b32 v7, a12
	v_accvgpr_read_b32 v6, a13
	ds_write2_b32 v8, v5, v4 offset0:168 offset1:204
	v_or3_b32 v4, v10, v0, s16
	v_mov_b32_e32 v1, 0
	v_fma_f32 v22, s6, v22, 0
	v_fma_f32 v21, s6, v21, 0
	v_fma_f32 v18, s6, v18, 0
	v_fma_f32 v17, s6, v17, 0
	v_fma_f32 v14, s6, v14, 0
	v_fma_f32 v13, s6, v13, 0
	v_fma_f32 v7, s6, v7, 0
	v_fma_f32 v6, s6, v6, 0
	v_cmp_gt_i32_e32 vcc, s4, v4
	ds_write2_b32 v12, v22, v21 offset1:36
	ds_write2_b32 v19, v18, v17 offset0:32 offset1:68
	ds_write2_b32 v15, v14, v13 offset0:64 offset1:100
	ds_write2_b32 v8, v7, v6 offset0:96 offset1:132
	s_and_saveexec_b64 s[2:3], vcc
	s_cbranch_execz .LBB11_9
	s_load_dwordx4 s[0:3], s[0:1], 0x40
	s_ashr_i32 s4, s17, 31
	v_lshlrev_b32_e32 v4, 2, v0
	v_add_u32_e32 v0, s7, v11
	v_ashrrev_i32_e32 v5, 31, v0
	s_waitcnt lgkmcnt(0)
	s_mul_hi_u32 s5, s2, s17
	s_mul_i32 s4, s2, s4
	s_mul_i32 s3, s3, s17
	s_add_i32 s4, s5, s4
	s_add_i32 s3, s4, s3
	s_mul_i32 s2, s2, s17
	s_lshl_b64 s[2:3], s[2:3], 2
	s_add_u32 s2, s8, s2
	v_mul_lo_u32 v5, s0, v5
	v_mul_lo_u32 v8, s1, v0
	v_mad_u64_u32 v[6:7], s[4:5], s0, v0, 0
	s_addc_u32 s3, s9, s3
	v_add3_u32 v7, v7, v5, v8
	v_lshl_add_u64 v[6:7], v[6:7], 2, s[2:3]
	s_ashr_i32 s17, s16, 31
	v_lshl_add_u64 v[6:7], s[16:17], 2, v[6:7]
	v_lshlrev_b32_e32 v0, 2, v10
	v_lshrrev_b32_e32 v12, 3, v2
	v_lshl_add_u64 v[6:7], v[6:7], 0, v[0:1]
	v_mul_u32_u24_e32 v0, 0x90, v12
	v_mov_b32_e32 v5, v1
	v_add3_u32 v13, v3, v4, v0
	v_lshl_add_u64 v[8:9], v[6:7], 0, v[4:5]
	ds_read_b128 v[0:3], v13
	v_mad_u64_u32 v[4:5], s[2:3], s0, v12, 0
	v_mov_b32_e32 v6, v5
	v_mad_u64_u32 v[6:7], s[2:3], s1, v12, v[6:7]
	v_mov_b32_e32 v5, v6
	v_lshl_add_u64 v[10:11], v[4:5], 2, v[8:9]
	ds_read_b128 v[4:7], v13 offset:1152
	s_waitcnt lgkmcnt(1)
	global_store_dwordx4 v[10:11], v[0:3], off sc1
	s_nop 1
	v_or_b32_e32 v3, 8, v12
	v_mad_u64_u32 v[0:1], s[2:3], s0, v3, 0
	v_mov_b32_e32 v2, v1
	v_mad_u64_u32 v[2:3], s[2:3], s1, v3, v[2:3]
	v_mov_b32_e32 v1, v2
	v_lshl_add_u64 v[0:1], v[0:1], 2, v[8:9]
	s_waitcnt lgkmcnt(0)
	global_store_dwordx4 v[0:1], v[4:7], off sc1
	ds_read_b128 v[0:3], v13 offset:2304
	s_nop 0
	v_or_b32_e32 v7, 16, v12
	v_mad_u64_u32 v[4:5], s[2:3], s0, v7, 0
	v_mov_b32_e32 v6, v5
	v_mad_u64_u32 v[6:7], s[2:3], s1, v7, v[6:7]
	v_mov_b32_e32 v5, v6
	v_lshl_add_u64 v[10:11], v[4:5], 2, v[8:9]
	ds_read_b128 v[4:7], v13 offset:3456
	s_waitcnt lgkmcnt(1)
	global_store_dwordx4 v[10:11], v[0:3], off sc1
	s_nop 1
	v_or_b32_e32 v3, 24, v12
	v_mad_u64_u32 v[0:1], s[2:3], s0, v3, 0
	v_mov_b32_e32 v2, v1
	v_mad_u64_u32 v[2:3], s[0:1], s1, v3, v[2:3]
	v_mov_b32_e32 v1, v2
	v_lshl_add_u64 v[0:1], v[0:1], 2, v[8:9]
	s_waitcnt lgkmcnt(0)
	global_store_dwordx4 v[0:1], v[4:7], off sc1
.LBB11_9:
	s_endpgm
	s_endpgm
	s_endpgm
	s_endpgm
	s_endpgm
	s_endpgm
	s_endpgm
	s_endpgm
	s_endpgm
	s_endpgm
	s_endpgm
	s_endpgm
	s_endpgm
	s_endpgm
	s_endpgm
	s_endpgm
	s_endpgm
	s_endpgm
	s_endpgm
	s_endpgm
	s_endpgm
	s_endpgm
	s_endpgm
	s_endpgm
	s_endpgm
	s_endpgm
	s_endpgm
	s_endpgm
	s_endpgm
	s_endpgm
	s_endpgm
	s_endpgm
	s_endpgm
	s_endpgm
	s_endpgm
	s_endpgm
	s_endpgm
	s_endpgm
	s_endpgm
	s_endpgm
	s_endpgm
	.section	.rodata,"a",@progbits
	.p2align	6, 0x0

.LBB18_6:
	s_or_b64 exec, exec, s[2:3]
	s_xor_b32 s2, s20, s19
	s_mul_i32 s19, s22, s17
	s_sub_i32 s19, s21, s19
	s_add_i32 s20, s22, 1
	s_sub_i32 s21, s19, s17
	s_cmp_ge_u32 s19, s17
	s_cselect_b32 s20, s20, s22
	s_cselect_b32 s19, s21, s19
	s_add_i32 s21, s20, 1
	s_cmp_ge_u32 s19, s17
	s_cselect_b32 s17, s21, s20
	s_xor_b32 s17, s17, s2
	s_sub_i32 s17, s17, s2
	s_load_dwordx2 s[24:25], s[0:1], 0x10
	s_load_dword s3, s[0:1], 0x28
	s_mul_i32 s2, s17, s16
	s_sub_i32 s2, s18, s2
	v_lshlrev_b32_e32 v2, 3, v0
	s_mul_i32 s16, s17, s5
	s_lshl_b32 s2, s2, 6
	v_lshrrev_b32_e32 v15, 2, v0
	v_and_b32_e32 v2, 24, v2
	s_ashr_i32 s17, s16, 31
	v_or_b32_e32 v8, s2, v15
	s_ashr_i32 s18, s2, 31
	v_lshl_add_u64 v[4:5], s[16:17], 0, v[2:3]
	s_waitcnt lgkmcnt(0)
	s_mul_i32 s18, s24, s18
	v_mad_u64_u32 v[6:7], s[16:17], s24, v8, v[4:5]
	v_mul_lo_u32 v3, s25, v8
	v_add3_u32 v7, v3, v7, s18
	v_add_u32_e32 v3, s7, v15
	s_add_i32 s4, s4, -1
	v_min_i32_e32 v3, s4, v3
	v_mad_i64_i32 v[8:9], s[16:17], v3, s3, v[4:5]
	v_lshlrev_b64 v[8:9], 1, v[8:9]
	v_lshlrev_b64 v[10:11], 1, v[6:7]
	v_lshl_add_u64 v[6:7], s[12:13], 0, v[8:9]
	global_load_dwordx4 v[70:73], v[6:7], off
	v_lshl_add_u64 v[8:9], s[14:15], 0, v[8:9]
	v_lshl_add_u64 v[4:5], s[8:9], 0, v[10:11]
	global_load_dwordx4 v[74:77], v[8:9], off
	global_load_dwordx4 v[78:81], v[4:5], off
	v_lshl_add_u64 v[10:11], s[10:11], 0, v[10:11]
	global_load_dwordx4 v[82:85], v[10:11], off
	v_and_b32_e32 v3, 32, v15
	v_mul_u32_u24_e32 v15, 40, v15
	v_lshlrev_b32_e32 v17, 1, v2
	v_bfe_u32 v14, v0, 5, 1
	v_lshl_add_u32 v15, v15, 1, v17
	s_ashr_i32 s3, s5, 31
	s_lshr_b32 s3, s3, 27
	s_add_i32 s3, s5, s3
	s_ashr_i32 s3, s3, 5
	s_add_i32 s4, s3, -1
	s_min_i32 s5, s4, 2
	s_lshl_b32 s8, s5, 5
	s_ashr_i32 s9, s8, 31
	global_load_dwordx4 v[18:21], v[4:5], off offset:64
	global_load_dwordx4 v[22:25], v[10:11], off offset:64
	global_load_dwordx4 v[26:29], v[6:7], off offset:64
	global_load_dwordx4 v[34:37], v[8:9], off offset:64
	s_lshl_b64 s[8:9], s[8:9], 1
	v_lshl_add_u64 v[30:31], v[4:5], 0, s[8:9]
	v_lshl_add_u64 v[38:39], v[10:11], 0, s[8:9]
	v_lshl_add_u64 v[42:43], v[6:7], 0, s[8:9]
	v_lshl_add_u64 v[46:47], v[8:9], 0, s[8:9]
	global_load_dwordx4 v[30:33], v[30:31], off
	v_lshlrev_b32_e32 v66, 4, v14
	global_load_dwordx4 v[38:41], v[38:39], off
	s_movk_i32 s5, 0x50
	global_load_dwordx4 v[42:45], v[42:43], off
	v_or_b32_e32 v17, v3, v13
	global_load_dwordx4 v[46:49], v[46:47], off
	v_accvgpr_write_b32 a0, 0
	v_accvgpr_write_b32 a1, 0
	v_accvgpr_write_b32 a2, 0
	v_accvgpr_write_b32 a3, 0
	v_accvgpr_write_b32 a4, 0
	v_accvgpr_write_b32 a5, 0
	v_accvgpr_write_b32 a6, 0
	v_accvgpr_write_b32 a7, 0
	v_accvgpr_write_b32 a8, 0
	v_accvgpr_write_b32 a9, 0
	v_accvgpr_write_b32 a10, 0
	v_accvgpr_write_b32 a11, 0
	v_accvgpr_write_b32 a12, 0
	v_accvgpr_write_b32 a13, 0
	v_accvgpr_write_b32 a14, 0
	v_accvgpr_write_b32 a15, 0
	s_waitcnt vmcnt(11)
	ds_write_b128 v15, v[70:73] offset:10240
	s_waitcnt vmcnt(10)
	ds_write_b128 v15, v[74:77] offset:15360
	s_waitcnt vmcnt(9)
	ds_write_b128 v15, v[78:81]
	s_waitcnt vmcnt(8)
	ds_write_b128 v15, v[82:85] offset:5120
	s_waitcnt lgkmcnt(0)
	s_barrier
	v_mul_u32_u24_e32 v67, 0x50, v16
	v_mad_u32_u24 v16, v16, s5, v66
	v_mul_u32_u24_e32 v68, 0x50, v17
	v_mad_u32_u24 v17, v17, s5, v66
	ds_read_b128 v[58:61], v16 offset:15360
	ds_read_b128 v[50:53], v16 offset:10240
	ds_read_b128 v[54:57], v17
	ds_read_b128 v[62:65], v17 offset:5120
	s_nop 7
	s_mov_b32 s5, 0
	v_add_u32_e32 v16, v66, v68
	v_add_u32_e32 v17, v66, v67
	s_add_i32 s89, s3, -6
	s_cmp_gt_i32 s5, s89
	s_cbranch_scc1 .Ltail_LBB18x8
.LBB18_8:
	s_waitcnt lgkmcnt(0)
	v_mfma_f32_32x32x16_f16 a[0:15], v[62:65], v[50:53], a[0:15]
	ds_read_b128 v[66:69], v17 offset:10272
	ds_read_b128 v[70:73], v16 offset:5152
	ds_read_b128 v[74:77], v16 offset:32
	s_waitcnt vmcnt(7)
	ds_write_b128 v15, v[18:21] offset:20480
	s_waitcnt vmcnt(6)
	ds_write_b128 v15, v[22:25] offset:25600
	s_waitcnt vmcnt(5)
	ds_write_b128 v15, v[26:29] offset:30720
	v_mfma_f32_32x32x16_f16 a[0:15], v[54:57], v[58:61], a[0:15]
	ds_read_b128 v[62:65], v17 offset:15392
	s_waitcnt vmcnt(4)
	ds_write_b128 v15, v[34:37] offset:35840
	v_mfma_f32_32x32x16_f16 a[0:15], v[54:57], v[50:53], a[0:15]
	s_add_i32 s8, s5, 3
	s_min_i32 s8, s8, s4
	s_lshl_b32 s8, s8, 5
	s_ashr_i32 s9, s8, 31
	s_lshl_b64 s[8:9], s[8:9], 1
	v_lshl_add_u64 v[50:51], v[4:5], 0, s[8:9]
	s_waitcnt lgkmcnt(0)
	s_barrier
	v_lshl_add_u64 v[34:35], v[6:7], 0, s[8:9]
	v_lshl_add_u64 v[36:37], v[10:11], 0, s[8:9]
	global_load_dwordx4 v[18:21], v[50:51], off
	global_load_dwordx4 v[22:25], v[36:37], off
	global_load_dwordx4 v[26:29], v[34:35], off
	v_mfma_f32_32x32x16_f16 a[0:15], v[70:73], v[66:69], a[0:15]
	ds_read_b128 v[50:53], v17 offset:30720
	ds_read_b128 v[54:57], v16 offset:25600
	ds_read_b128 v[58:61], v16 offset:20480
	v_lshl_add_u64 v[34:35], v[8:9], 0, s[8:9]
	global_load_dwordx4 v[34:37], v[34:35], off
	v_mfma_f32_32x32x16_f16 a[0:15], v[74:77], v[62:65], a[0:15]
	ds_read_b128 v[70:73], v17 offset:35840
	v_mfma_f32_32x32x16_f16 a[0:15], v[74:77], v[66:69], a[0:15]
	s_waitcnt lgkmcnt(2)
	v_mfma_f32_32x32x16_f16 a[0:15], v[54:57], v[50:53], a[0:15]
	ds_read_b128 v[66:69], v17 offset:30752
	ds_read_b128 v[74:77], v16 offset:25632
	ds_read_b128 v[78:81], v16 offset:20512
	s_waitcnt vmcnt(7)
	ds_write_b128 v15, v[30:33]
	s_waitcnt vmcnt(6)
	ds_write_b128 v15, v[38:41] offset:5120
	s_waitcnt vmcnt(5)
	ds_write_b128 v15, v[42:45] offset:10240
	s_waitcnt lgkmcnt(6)
	v_mfma_f32_32x32x16_f16 a[0:15], v[58:61], v[70:73], a[0:15]
	ds_read_b128 v[82:85], v17 offset:35872
	s_waitcnt vmcnt(4)
	ds_write_b128 v15, v[46:49] offset:15360
	v_mfma_f32_32x32x16_f16 a[0:15], v[58:61], v[50:53], a[0:15]
	s_add_i32 s8, s5, 4
	s_min_i32 s8, s8, s4
	s_lshl_b32 s8, s8, 5
	s_ashr_i32 s9, s8, 31
	s_lshl_b64 s[8:9], s[8:9], 1
	v_lshl_add_u64 v[50:51], v[4:5], 0, s[8:9]
	s_waitcnt lgkmcnt(0)
	s_barrier
	v_lshl_add_u64 v[46:47], v[6:7], 0, s[8:9]
	v_lshl_add_u64 v[48:49], v[10:11], 0, s[8:9]
	global_load_dwordx4 v[30:33], v[50:51], off
	global_load_dwordx4 v[38:41], v[48:49], off
	global_load_dwordx4 v[42:45], v[46:47], off
	v_mfma_f32_32x32x16_f16 a[0:15], v[74:77], v[66:69], a[0:15]
	ds_read_b128 v[50:53], v17 offset:10240
	ds_read_b128 v[62:65], v16 offset:5120
	ds_read_b128 v[54:57], v16
	v_lshl_add_u64 v[46:47], v[8:9], 0, s[8:9]
	global_load_dwordx4 v[46:49], v[46:47], off
	v_mfma_f32_32x32x16_f16 a[0:15], v[78:81], v[82:85], a[0:15]
	ds_read_b128 v[58:61], v17 offset:15360
	v_mfma_f32_32x32x16_f16 a[0:15], v[78:81], v[66:69], a[0:15]
	s_add_i32 s5, s5, 2
	s_add_i32 s89, s3, -6
	s_cmp_le_i32 s5, s89
	s_cbranch_scc1 .LBB18_8
.Ltail_LBB18x8:
	s_waitcnt lgkmcnt(0)
	v_mfma_f32_32x32x16_f16 a[0:15], v[62:65], v[50:53], a[0:15]
	ds_read_b128 v[66:69], v17 offset:10272
	ds_read_b128 v[70:73], v16 offset:5152
	ds_read_b128 v[74:77], v16 offset:32
	s_waitcnt vmcnt(7)
	ds_write_b128 v15, v[18:21] offset:20480
	s_waitcnt vmcnt(6)
	ds_write_b128 v15, v[22:25] offset:25600
	s_waitcnt vmcnt(5)
	ds_write_b128 v15, v[26:29] offset:30720
	v_mfma_f32_32x32x16_f16 a[0:15], v[54:57], v[58:61], a[0:15]
	ds_read_b128 v[62:65], v17 offset:15392
	s_waitcnt vmcnt(4)
	ds_write_b128 v15, v[34:37] offset:35840
	v_mfma_f32_32x32x16_f16 a[0:15], v[54:57], v[50:53], a[0:15]
	s_add_i32 s8, s5, 3
	s_min_i32 s8, s8, s4
	s_lshl_b32 s8, s8, 5
	s_ashr_i32 s9, s8, 31
	s_lshl_b64 s[8:9], s[8:9], 1
	v_lshl_add_u64 v[50:51], v[4:5], 0, s[8:9]
	s_waitcnt lgkmcnt(0)
	s_barrier
	v_lshl_add_u64 v[34:35], v[6:7], 0, s[8:9]
	v_lshl_add_u64 v[36:37], v[10:11], 0, s[8:9]
	global_load_dwordx4 v[18:21], v[50:51], off
	global_load_dwordx4 v[22:25], v[36:37], off
	global_load_dwordx4 v[26:29], v[34:35], off
	v_mfma_f32_32x32x16_f16 a[0:15], v[70:73], v[66:69], a[0:15]
	ds_read_b128 v[50:53], v17 offset:30720
	ds_read_b128 v[54:57], v16 offset:25600
	ds_read_b128 v[58:61], v16 offset:20480
	v_lshl_add_u64 v[34:35], v[8:9], 0, s[8:9]
	global_load_dwordx4 v[34:37], v[34:35], off
	v_mfma_f32_32x32x16_f16 a[0:15], v[74:77], v[62:65], a[0:15]
	ds_read_b128 v[70:73], v17 offset:35840
	v_mfma_f32_32x32x16_f16 a[0:15], v[74:77], v[66:69], a[0:15]
	s_waitcnt lgkmcnt(2)
	v_mfma_f32_32x32x16_f16 a[0:15], v[54:57], v[50:53], a[0:15]
	ds_read_b128 v[66:69], v17 offset:30752
	ds_read_b128 v[74:77], v16 offset:25632
	ds_read_b128 v[78:81], v16 offset:20512
	s_waitcnt vmcnt(7)
	ds_write_b128 v15, v[30:33]
	s_waitcnt vmcnt(6)
	ds_write_b128 v15, v[38:41] offset:5120
	s_waitcnt vmcnt(5)
	ds_write_b128 v15, v[42:45] offset:10240
	s_waitcnt lgkmcnt(6)
	v_mfma_f32_32x32x16_f16 a[0:15], v[58:61], v[70:73], a[0:15]
	ds_read_b128 v[82:85], v17 offset:35872
	s_waitcnt vmcnt(4)
	ds_write_b128 v15, v[46:49] offset:15360
	v_mfma_f32_32x32x16_f16 a[0:15], v[58:61], v[50:53], a[0:15]
	s_add_i32 s8, s5, 4
	s_min_i32 s8, s8, s4
	s_lshl_b32 s8, s8, 5
	s_ashr_i32 s9, s8, 31
	s_lshl_b64 s[8:9], s[8:9], 1
	v_lshl_add_u64 v[50:51], v[4:5], 0, s[8:9]
	s_waitcnt lgkmcnt(0)
	s_barrier
	v_lshl_add_u64 v[46:47], v[6:7], 0, s[8:9]
	v_lshl_add_u64 v[48:49], v[10:11], 0, s[8:9]
	v_mfma_f32_32x32x16_f16 a[0:15], v[74:77], v[66:69], a[0:15]
	ds_read_b128 v[50:53], v17 offset:10240
	ds_read_b128 v[62:65], v16 offset:5120
	ds_read_b128 v[54:57], v16
	v_lshl_add_u64 v[46:47], v[8:9], 0, s[8:9]
	v_mfma_f32_32x32x16_f16 a[0:15], v[78:81], v[82:85], a[0:15]
	ds_read_b128 v[58:61], v17 offset:15360
	v_mfma_f32_32x32x16_f16 a[0:15], v[78:81], v[66:69], a[0:15]
	s_add_i32 s5, s5, 2
	s_waitcnt lgkmcnt(0)
	v_mfma_f32_32x32x16_f16 a[0:15], v[62:65], v[50:53], a[0:15]
	ds_read_b128 v[66:69], v17 offset:10272
	ds_read_b128 v[70:73], v16 offset:5152
	ds_read_b128 v[74:77], v16 offset:32
	s_waitcnt vmcnt(3)
	ds_write_b128 v15, v[18:21] offset:20480
	s_waitcnt vmcnt(2)
	ds_write_b128 v15, v[22:25] offset:25600
	s_waitcnt vmcnt(1)
	ds_write_b128 v15, v[26:29] offset:30720
	v_mfma_f32_32x32x16_f16 a[0:15], v[54:57], v[58:61], a[0:15]
	ds_read_b128 v[62:65], v17 offset:15392
	s_waitcnt vmcnt(0)
	ds_write_b128 v15, v[34:37] offset:35840
	v_mfma_f32_32x32x16_f16 a[0:15], v[54:57], v[50:53], a[0:15]
	s_add_i32 s8, s5, 3
	s_min_i32 s8, s8, s4
	s_lshl_b32 s8, s8, 5
	s_ashr_i32 s9, s8, 31
	s_lshl_b64 s[8:9], s[8:9], 1
	v_lshl_add_u64 v[50:51], v[4:5], 0, s[8:9]
	s_waitcnt lgkmcnt(0)
	s_barrier
	v_lshl_add_u64 v[34:35], v[6:7], 0, s[8:9]
	v_lshl_add_u64 v[36:37], v[10:11], 0, s[8:9]
	v_mfma_f32_32x32x16_f16 a[0:15], v[70:73], v[66:69], a[0:15]
	ds_read_b128 v[50:53], v17 offset:30720
	ds_read_b128 v[54:57], v16 offset:25600
	ds_read_b128 v[58:61], v16 offset:20480
	v_lshl_add_u64 v[34:35], v[8:9], 0, s[8:9]
	v_mfma_f32_32x32x16_f16 a[0:15], v[74:77], v[62:65], a[0:15]
	ds_read_b128 v[70:73], v17 offset:35840
	v_mfma_f32_32x32x16_f16 a[0:15], v[74:77], v[66:69], a[0:15]
	s_waitcnt lgkmcnt(2)
	v_mfma_f32_32x32x16_f16 a[0:15], v[54:57], v[50:53], a[0:15]
	ds_read_b128 v[66:69], v17 offset:30752
	ds_read_b128 v[74:77], v16 offset:25632
	ds_read_b128 v[78:81], v16 offset:20512
	ds_write_b128 v15, v[30:33]
	ds_write_b128 v15, v[38:41] offset:5120
	ds_write_b128 v15, v[42:45] offset:10240
	s_waitcnt lgkmcnt(6)
	v_mfma_f32_32x32x16_f16 a[0:15], v[58:61], v[70:73], a[0:15]
	ds_read_b128 v[82:85], v17 offset:35872
	ds_write_b128 v15, v[46:49] offset:15360
	v_mfma_f32_32x32x16_f16 a[0:15], v[58:61], v[50:53], a[0:15]
	s_add_i32 s8, s5, 4
	s_min_i32 s8, s8, s4
	s_lshl_b32 s8, s8, 5
	s_ashr_i32 s9, s8, 31
	s_lshl_b64 s[8:9], s[8:9], 1
	v_lshl_add_u64 v[50:51], v[4:5], 0, s[8:9]
	s_waitcnt lgkmcnt(0)
	s_barrier
	v_lshl_add_u64 v[46:47], v[6:7], 0, s[8:9]
	v_lshl_add_u64 v[48:49], v[10:11], 0, s[8:9]
	v_mfma_f32_32x32x16_f16 a[0:15], v[74:77], v[66:69], a[0:15]
	ds_read_b128 v[50:53], v17 offset:10240
	ds_read_b128 v[62:65], v16 offset:5120
	ds_read_b128 v[54:57], v16
	v_lshl_add_u64 v[46:47], v[8:9], 0, s[8:9]
	v_mfma_f32_32x32x16_f16 a[0:15], v[78:81], v[82:85], a[0:15]
	ds_read_b128 v[58:61], v17 offset:15360
	v_mfma_f32_32x32x16_f16 a[0:15], v[78:81], v[66:69], a[0:15]
.LBB18_9:
	s_waitcnt vmcnt(0)
	s_waitcnt vmcnt(7)
	s_nop 7
	v_accvgpr_read_b32 v21, a1
	v_mul_u32_u24_e32 v14, 0xa0, v14
	s_waitcnt vmcnt(6)
	v_accvgpr_read_b32 v22, a0
	v_or_b32_e32 v13, v14, v13
	v_fma_f32 v14, s6, v21, v12
	v_lshrrev_b32_e32 v23, 6, v0
	v_fma_f32 v22, s6, v22, v12
	s_mov_b32 s3, 0x43800000
	v_max_f32_e32 v14, 0, v14
	v_mul_u32_u24_e32 v23, 0x1400, v23
	v_max_f32_e32 v22, 0, v22
	v_fma_mixlo_f16 v21, v14, s3, 0
	v_accvgpr_read_b32 v20, a2
	v_fma_mixlo_f16 v24, v22, s3, 0
	v_lshl_or_b32 v13, v13, 1, v23
	v_fma_mixlo_f16 v14, v14, s3, -v21 op_sel_hi:[0,0,1]
	s_load_dwordx4 s[8:11], s[0:1], 0x50
	v_fma_mixlo_f16 v22, v22, s3, -v24 op_sel_hi:[0,0,1]
	s_load_dwordx2 s[0:1], s[0:1], 0x40
	s_waitcnt lgkmcnt(0)
	s_barrier
	ds_write_b16 v13, v24
	ds_write_b16 v13, v22 offset:2560
	ds_write_b16 v13, v21 offset:80
	ds_write_b16 v13, v14 offset:2640
	v_fma_f32 v14, s6, v20, v12
	v_max_f32_e32 v14, 0, v14
	v_fma_mixlo_f16 v20, v14, s3, 0
	v_accvgpr_read_b32 v19, a3
	v_fma_mixlo_f16 v14, v14, s3, -v20 op_sel_hi:[0,0,1]
	ds_write_b16 v13, v20 offset:160
	ds_write_b16 v13, v14 offset:2720
	v_fma_f32 v14, s6, v19, v12
	v_max_f32_e32 v14, 0, v14
	v_fma_mixlo_f16 v19, v14, s3, 0
	v_accvgpr_read_b32 v18, a4
	v_fma_mixlo_f16 v14, v14, s3, -v19 op_sel_hi:[0,0,1]
	ds_write_b16 v13, v19 offset:240
	ds_write_b16 v13, v14 offset:2800
	v_fma_f32 v14, s6, v18, v12
	v_max_f32_e32 v14, 0, v14
	v_fma_mixlo_f16 v18, v14, s3, 0
	v_accvgpr_read_b32 v17, a5
	v_fma_mixlo_f16 v14, v14, s3, -v18 op_sel_hi:[0,0,1]
	ds_write_b16 v13, v18 offset:640
	ds_write_b16 v13, v14 offset:3200
	v_fma_f32 v14, s6, v17, v12
	v_max_f32_e32 v14, 0, v14
	v_fma_mixlo_f16 v17, v14, s3, 0
	v_accvgpr_read_b32 v16, a6
	v_fma_mixlo_f16 v14, v14, s3, -v17 op_sel_hi:[0,0,1]
	ds_write_b16 v13, v17 offset:720
	ds_write_b16 v13, v14 offset:3280
	v_fma_f32 v14, s6, v16, v12
	v_max_f32_e32 v14, 0, v14
	v_fma_mixlo_f16 v16, v14, s3, 0
	v_accvgpr_read_b32 v15, a7
	v_fma_mixlo_f16 v14, v14, s3, -v16 op_sel_hi:[0,0,1]
	ds_write_b16 v13, v16 offset:800
	ds_write_b16 v13, v14 offset:3360
	v_fma_f32 v14, s6, v15, v12
	v_accvgpr_read_b32 v11, a8
	v_max_f32_e32 v14, 0, v14
	v_fma_mixlo_f16 v15, v14, s3, 0
	v_fma_f32 v11, s6, v11, v12
	v_accvgpr_read_b32 v10, a9
	v_fma_mixlo_f16 v14, v14, s3, -v15 op_sel_hi:[0,0,1]
	v_max_f32_e32 v11, 0, v11
	ds_write_b16 v13, v15 offset:880
	ds_write_b16 v13, v14 offset:3440
	v_fma_mixlo_f16 v14, v11, s3, 0
	v_fma_f32 v10, s6, v10, v12
	v_accvgpr_read_b32 v9, a10
	v_fma_mixlo_f16 v11, v11, s3, -v14 op_sel_hi:[0,0,1]
	v_max_f32_e32 v10, 0, v10
	ds_write_b16 v13, v14 offset:1280
	ds_write_b16 v13, v11 offset:3840
	v_fma_mixlo_f16 v11, v10, s3, 0
	v_fma_f32 v9, s6, v9, v12
	v_accvgpr_read_b32 v8, a11
	v_fma_mixlo_f16 v10, v10, s3, -v11 op_sel_hi:[0,0,1]
	v_max_f32_e32 v9, 0, v9
	ds_write_b16 v13, v11 offset:1360
	ds_write_b16 v13, v10 offset:3920
	v_fma_mixlo_f16 v10, v9, s3, 0
	v_fma_f32 v8, s6, v8, v12
	v_accvgpr_read_b32 v7, a12
	v_fma_mixlo_f16 v9, v9, s3, -v10 op_sel_hi:[0,0,1]
	v_max_f32_e32 v8, 0, v8
	ds_write_b16 v13, v10 offset:1440
	ds_write_b16 v13, v9 offset:4000
	v_fma_mixlo_f16 v9, v8, s3, 0
	v_fma_f32 v7, s6, v7, v12
	v_accvgpr_read_b32 v6, a13
	v_fma_mixlo_f16 v8, v8, s3, -v9 op_sel_hi:[0,0,1]
	v_max_f32_e32 v7, 0, v7
	ds_write_b16 v13, v9 offset:1520
	ds_write_b16 v13, v8 offset:4080
	v_fma_mixlo_f16 v8, v7, s3, 0
	v_fma_f32 v6, s6, v6, v12
	v_accvgpr_read_b32 v5, a14
	v_fma_mixlo_f16 v7, v7, s3, -v8 op_sel_hi:[0,0,1]
	v_max_f32_e32 v6, 0, v6
	ds_write_b16 v13, v8 offset:1920
	ds_write_b16 v13, v7 offset:4480
	v_fma_mixlo_f16 v7, v6, s3, 0
	v_fma_f32 v5, s6, v5, v12
	v_accvgpr_read_b32 v4, a15
	v_fma_mixlo_f16 v6, v6, s3, -v7 op_sel_hi:[0,0,1]
	v_max_f32_e32 v5, 0, v5
	ds_write_b16 v13, v7 offset:2000
	ds_write_b16 v13, v6 offset:4560
	v_fma_mixlo_f16 v6, v5, s3, 0
	v_fmac_f32_e32 v12, s6, v4
	v_fma_mixlo_f16 v5, v5, s3, -v6 op_sel_hi:[0,0,1]
	v_max_f32_e32 v4, 0, v12
	ds_write_b16 v13, v6 offset:2080
	ds_write_b16 v13, v5 offset:4640
	v_fma_mixlo_f16 v5, v4, s3, 0
	v_and_b32_e32 v0, 63, v0
	v_fma_mixlo_f16 v4, v4, s3, -v5 op_sel_hi:[0,0,1]
	v_add_u32_e32 v3, s2, v3
	s_ashr_i32 s2, s7, 31
	ds_write_b16 v13, v5 offset:2160
	ds_write_b16 v13, v4 offset:4720
	v_lshrrev_b32_e32 v20, 2, v0
	v_ashrrev_i32_e32 v4, 31, v3
	v_or3_b32 v0, v1, v2, s7
	v_mov_b32_e32 v1, s2
	v_mul_lo_u32 v4, s0, v4
	v_mad_u64_u32 v[0:1], s[2:3], s0, v3, v[0:1]
	v_mul_lo_u32 v3, s1, v3
	v_add3_u32 v1, v3, v1, v4
	v_lshlrev_b64 v[0:1], 1, v[0:1]
	v_lshl_or_b32 v2, v2, 1, v23
	v_lshl_add_u64 v[12:13], s[8:9], 0, v[0:1]
	v_lshl_add_u64 v[14:15], s[10:11], 0, v[0:1]
	v_mul_u32_u24_e32 v0, 40, v20
	v_lshl_add_u32 v21, v0, 1, v2
	v_mad_u64_u32 v[8:9], s[2:3], s0, v20, 0
	ds_read_b128 v[0:3], v21
	ds_read_b128 v[4:7], v21 offset:2560
	v_mov_b32_e32 v10, v9
	v_mad_u64_u32 v[10:11], s[2:3], s1, v20, v[10:11]
	v_mov_b32_e32 v9, v10
	v_lshlrev_b64 v[16:17], 1, v[8:9]
	v_lshl_add_u64 v[18:19], v[12:13], 0, v[16:17]
	v_lshl_add_u64 v[16:17], v[14:15], 0, v[16:17]
	s_waitcnt lgkmcnt(0)
	global_store_dwordx4 v[16:17], v[4:7], off sc1
	ds_read_b128 v[8:11], v21 offset:1280
	global_store_dwordx4 v[18:19], v[0:3], off sc1
	v_or_b32_e32 v7, 16, v20
	v_mad_u64_u32 v[4:5], s[2:3], s0, v7, 0
	ds_read_b128 v[0:3], v21 offset:3840
	v_mov_b32_e32 v6, v5
	v_mad_u64_u32 v[6:7], s[0:1], s1, v7, v[6:7]
	v_mov_b32_e32 v5, v6
	v_lshlrev_b64 v[4:5], 1, v[4:5]
	v_lshl_add_u64 v[6:7], v[12:13], 0, v[4:5]
	v_lshl_add_u64 v[4:5], v[14:15], 0, v[4:5]
	s_waitcnt lgkmcnt(1)
	global_store_dwordx4 v[6:7], v[8:11], off sc1
	s_waitcnt lgkmcnt(0)
	global_store_dwordx4 v[4:5], v[0:3], off sc1
	s_endpgm
	s_endpgm
	s_endpgm
	s_endpgm
	s_endpgm
	s_endpgm
	s_endpgm
	s_endpgm
	s_endpgm
	s_endpgm
	s_endpgm
	s_endpgm
	s_endpgm
	s_endpgm
	s_endpgm
	s_endpgm
	s_endpgm
	s_endpgm
	s_endpgm
	s_endpgm
	s_endpgm
	s_endpgm
	s_endpgm
	s_endpgm
	s_endpgm
	s_endpgm
	s_endpgm
	s_endpgm
	s_endpgm
	s_endpgm
	s_endpgm
